# as the TOP-polling version but the RWKV workgroups convert 6 (not 8) rows per wave of the layer-0 u table
# baseline (speedup 1.0000x reference)
; __device__ __forceinline__ void peer_row_load(f32x4 (&v)[16], const float* const (&in)[34], int it, int layer, int lane) {
;     const int tbl = it >= NEXP, r = it - tbl * NEXP + layer * NEXP;
;     const f32x4* src = (const f32x4*)((tbl ? in[33] : in[32]) + (size_t)r * D) + lane;
; #pragma unroll
;     for (int j = 0; j < 16; ++j) v[j] = src[64 * j];
; }
;     f32x4 va[16], vb[16];
;     if (it_lo + gw >= it_hi) return;
;     peer_row_load(va, in, it_lo + gw, only_layer, lane);
; #pragma unroll 1
;     for (int it = it_lo + gw; it < it_hi; it += 2 * NGW) {
;         const int it1 = it + NGW, it2 = it + 2 * NGW;
;         peer_row_load(vb, in, it1 < it_hi ? it1 : it, only_layer, lane);
.LBB0_618:
	v_mov_b32_e32 v1, v0
	s_nop 0
	v_readfirstlane_b32 s0, v1
	s_ashr_i32 s16, s0, 6
	s_lshl_b32 s0, s35, 3
	s_add_i32 s4, s16, s0
	v_and_b32_e32 v134, 63, v1
	s_cmpk_gt_i32 s4, 0x27ff
	v_lshlrev_b32_e32 v136, 2, v134
	v_cmp_eq_u32_e64 s[0:1], 0, v134
	s_cbranch_scc1 .LBB0_627
	s_ashr_i32 s5, s4, 31
	s_lshl_b64 s[6:7], s[4:5], 14
	s_add_u32 s6, s84, s6
	s_addc_u32 s7, s85, s7
	v_mov_b32_e32 v131, 0
	v_lshlrev_b32_e32 v130, 4, v134
	v_lshl_add_u64 v[2:3], s[6:7], 0, v[130:131]
	v_add_co_u32_e32 v4, vcc, 0x1000, v2
	global_load_dwordx4 v[86:89], v130, s[6:7]
	global_load_dwordx4 v[62:65], v130, s[6:7] offset:1024
	global_load_dwordx4 v[50:53], v130, s[6:7] offset:2048
	global_load_dwordx4 v[54:57], v130, s[6:7] offset:3072
	v_addc_co_u32_e32 v5, vcc, 0, v3, vcc
	global_load_dwordx4 v[46:49], v[4:5], off
	global_load_dwordx4 v[42:45], v[4:5], off offset:1024
	global_load_dwordx4 v[38:41], v[4:5], off offset:2048
	global_load_dwordx4 v[34:37], v[4:5], off offset:3072
	v_add_co_u32_e32 v4, vcc, 0x2000, v2
	v_mov_b32_e32 v137, v131
	s_nop 0
	v_addc_co_u32_e32 v5, vcc, 0, v3, vcc
	v_add_co_u32_e32 v2, vcc, 0x3000, v2
	global_load_dwordx4 v[30:33], v[4:5], off
	global_load_dwordx4 v[26:29], v[4:5], off offset:1024
	global_load_dwordx4 v[22:25], v[4:5], off offset:2048
	global_load_dwordx4 v[14:17], v[4:5], off offset:3072
	v_addc_co_u32_e32 v3, vcc, 0, v3, vcc
	global_load_dwordx4 v[18:21], v[2:3], off
	global_load_dwordx4 v[10:13], v[2:3], off offset:1024
	global_load_dwordx4 v[6:9], v[2:3], off offset:2048
	s_nop 0
	global_load_dwordx4 v[2:5], v[2:3], off offset:3072
	v_lshl_add_u64 v[58:59], s[90:91], 0, v[136:137]
	s_mov_b64 s[6:7], 0xba00000
	s_add_u32 s17, s90, 0x1ba00000
	v_lshl_add_u64 v[132:133], v[58:59], 0, s[6:7]
	s_addc_u32 s18, s91, 0
	s_lshl_b32 s6, s2, 3
	s_lshl_b32 s29, s34, 4
	s_lshl_b32 s30, s34, 3
	s_movk_i32 s5, 0x1000
	s_movk_i32 s14, 0x2000
	s_movk_i32 s15, 0x3000
	s_add_i32 s19, s16, s6
	s_add_i32 s28, s29, 0xfffff800
	s_addk_i32 s29, 0xf400
	s_addk_i32 s30, 0xf800
	s_mov_b32 s31, 0x43800000
	s_branch .LBB0_622

; __device__ __forceinline__ void peer_row_store(const f32x4 (&v)[16], unsigned char* ws, int it, int layer, int lane) {
;     const int tbl = it >= NEXP, r = it - tbl * NEXP + layer * NEXP;
;     float am = 0.f;
; #pragma unroll
;     for (int j = 0; j < 16; ++j) am = fmaxf(fmaxf(am, fmaxf(fabsf(v[j][0]), fabsf(v[j][1]))), fmaxf(fabsf(v[j][2]), fabsf(v[j][3])));
;     am = __uint_as_float(max64u(__float_as_uint(am)));
;     ...
;     for (int it = it_lo + gw; it < it_hi; it += 2 * NGW) {
;         const int it1 = it + NGW, it2 = it + 2 * NGW;
;         peer_row_load(vb, in, it1 < it_hi ? it1 : it, only_layer, lane);
;         __builtin_amdgcn_sched_barrier(0);
;         peer_row_store(va, ws, it, only_layer, lane);
;         __builtin_amdgcn_sched_barrier(0);
;         peer_row_load(va, in, it2 < it_hi ? it2 : it, only_layer, lane);
.LBB0_621:
	s_add_i32 s19, s19, s28
	s_add_i32 s6, s19, 0xfffffc00
	s_cmpk_lt_i32 s6, 0x2800
	s_cbranch_scc0 .LBB0_627
.LBB0_622:
	s_add_i32 s10, s19, 0xfffffc00
	s_add_i32 s6, s30, s19
	s_cmpk_lt_i32 s6, 0x2800
	s_cselect_b64 s[8:9], -1, 0
	s_and_b64 s[12:13], s[8:9], exec
	s_cselect_b32 s7, s6, s10
	s_cmpk_gt_i32 s7, 0x3fff
	s_cselect_b32 s11, 0xffffc000, 0
	s_cselect_b32 s20, s86, s84
	s_cselect_b32 s21, s87, s85
	s_add_i32 s12, s11, s7
	s_ashr_i32 s13, s12, 31
	s_lshl_b64 s[12:13], s[12:13], 14
	s_add_u32 s12, s20, s12
	s_addc_u32 s13, s21, s13
	v_lshlrev_b32_e32 v130, 4, v134
	s_waitcnt vmcnt(32)
	v_lshl_add_u64 v[58:59], s[12:13], 0, v[130:131]
	v_add_co_u32_e32 v60, vcc, s5, v58
	global_load_dwordx4 v[122:125], v130, s[12:13] offset:1024
	global_load_dwordx4 v[118:121], v130, s[12:13] offset:2048
	v_addc_co_u32_e32 v61, vcc, 0, v59, vcc
	v_add_co_u32_e32 v66, vcc, s14, v58
	s_nop 1
	v_addc_co_u32_e32 v67, vcc, 0, v59, vcc
	global_load_dwordx4 v[114:117], v130, s[12:13] offset:3072
	global_load_dwordx4 v[110:113], v[66:67], off offset:-4096
	global_load_dwordx4 v[106:109], v[60:61], off offset:1024
	global_load_dwordx4 v[102:105], v[60:61], off offset:2048
	global_load_dwordx4 v[94:97], v[66:67], off
	global_load_dwordx4 v[90:93], v[66:67], off offset:1024
	global_load_dwordx4 v[82:85], v[66:67], off offset:2048
	global_load_dwordx4 v[78:81], v[66:67], off offset:3072
	v_add_co_u32_e32 v58, vcc, s15, v58
	s_nop 1
	v_addc_co_u32_e32 v59, vcc, 0, v59, vcc
	global_load_dwordx4 v[98:101], v[60:61], off offset:3072
	global_load_dwordx4 v[74:77], v[58:59], off
	global_load_dwordx4 v[70:73], v[58:59], off offset:1024
	global_load_dwordx4 v[66:69], v[58:59], off offset:2048
	global_load_dwordx4 v[126:129], v130, s[12:13]
	s_nop 0
	global_load_dwordx4 v[58:61], v[58:59], off offset:3072
	s_waitcnt vmcnt(17)
	v_max_f32_e64 v135, |v87|, |v87|
	v_max_f32_e64 v137, |v86|, |v86|
	v_max_f32_e32 v135, v137, v135
	v_max_f32_e64 v137, |v89|, |v89|
	v_max_f32_e64 v138, |v88|, |v88|
	v_max_f32_e32 v137, v138, v137
	v_max3_f32 v135, v135, 0, v137
	s_waitcnt vmcnt(30)
	v_max_f32_e64 v137, |v63|, |v63|
	v_max_f32_e64 v138, |v62|, |v62|
	v_max_f32_e32 v137, v138, v137
	v_max_f32_e64 v138, |v65|, |v65|
	v_max_f32_e64 v139, |v64|, |v64|
	v_max_f32_e32 v138, v139, v138
	v_max3_f32 v135, v135, v137, v138
	s_waitcnt vmcnt(29)
	v_max_f32_e64 v137, |v51|, |v51|
	v_max_f32_e64 v138, |v50|, |v50|
	v_max_f32_e32 v137, v138, v137
	v_max_f32_e64 v138, |v53|, |v53|
	v_max_f32_e64 v139, |v52|, |v52|
	v_max_f32_e32 v138, v139, v138
	v_max3_f32 v135, v135, v137, v138
	s_waitcnt vmcnt(28)
	v_max_f32_e64 v137, |v55|, |v55|
	v_max_f32_e64 v138, |v54|, |v54|
	v_max_f32_e32 v137, v138, v137
	v_max_f32_e64 v138, |v57|, |v57|
	v_max_f32_e64 v139, |v56|, |v56|
	v_max_f32_e32 v138, v139, v138
	v_max3_f32 v135, v135, v137, v138
	s_waitcnt vmcnt(27)
	v_max_f32_e64 v137, |v47|, |v47|
	v_max_f32_e64 v138, |v46|, |v46|
	v_max_f32_e32 v137, v138, v137
	v_max_f32_e64 v138, |v49|, |v49|
	v_max_f32_e64 v139, |v48|, |v48|
	v_max_f32_e32 v138, v139, v138
	v_max3_f32 v135, v135, v137, v138
	s_waitcnt vmcnt(26)
	v_max_f32_e64 v137, |v43|, |v43|
	v_max_f32_e64 v138, |v42|, |v42|
	v_max_f32_e32 v137, v138, v137
	v_max_f32_e64 v138, |v45|, |v45|
	v_max_f32_e64 v139, |v44|, |v44|
	v_max_f32_e32 v138, v139, v138
	v_max3_f32 v135, v135, v137, v138
	s_waitcnt vmcnt(25)
	v_max_f32_e64 v137, |v39|, |v39|
	v_max_f32_e64 v138, |v38|, |v38|
	v_max_f32_e32 v137, v138, v137
	v_max_f32_e64 v138, |v41|, |v41|
	v_max_f32_e64 v139, |v40|, |v40|
	v_max_f32_e32 v138, v139, v138
	v_max3_f32 v135, v135, v137, v138
	s_waitcnt vmcnt(24)
	v_max_f32_e64 v137, |v35|, |v35|
	v_max_f32_e64 v138, |v34|, |v34|
	v_max_f32_e32 v137, v138, v137
	v_max_f32_e64 v138, |v37|, |v37|
	v_max_f32_e64 v139, |v36|, |v36|
	v_max_f32_e32 v138, v139, v138
	v_max3_f32 v135, v135, v137, v138
	s_waitcnt vmcnt(23)
	v_max_f32_e64 v137, |v31|, |v31|
	v_max_f32_e64 v138, |v30|, |v30|
	v_max_f32_e32 v137, v138, v137
	v_max_f32_e64 v138, |v33|, |v33|
	v_max_f32_e64 v139, |v32|, |v32|
	v_max_f32_e32 v138, v139, v138
	v_max3_f32 v135, v135, v137, v138
	s_waitcnt vmcnt(22)
	v_max_f32_e64 v137, |v27|, |v27|
	v_max_f32_e64 v138, |v26|, |v26|
	v_max_f32_e32 v137, v138, v137
	v_max_f32_e64 v138, |v29|, |v29|
	v_max_f32_e64 v139, |v28|, |v28|
	v_max_f32_e32 v138, v139, v138
	v_max3_f32 v135, v135, v137, v138
	s_waitcnt vmcnt(21)
	v_max_f32_e64 v137, |v23|, |v23|
	v_max_f32_e64 v138, |v22|, |v22|
	v_max_f32_e32 v137, v138, v137
	v_max_f32_e64 v138, |v25|, |v25|
	v_max_f32_e64 v139, |v24|, |v24|
	v_max_f32_e32 v138, v139, v138
	v_max3_f32 v135, v135, v137, v138
	s_waitcnt vmcnt(20)
	v_max_f32_e64 v137, |v15|, |v15|
	v_max_f32_e64 v138, |v14|, |v14|
	v_max_f32_e32 v137, v138, v137
	v_max_f32_e64 v138, |v17|, |v17|
	v_max_f32_e64 v139, |v16|, |v16|
	v_max_f32_e32 v138, v139, v138
	v_max3_f32 v135, v135, v137, v138
	s_waitcnt vmcnt(19)
	v_max_f32_e64 v137, |v19|, |v19|
	v_max_f32_e64 v138, |v18|, |v18|
	v_max_f32_e32 v137, v138, v137
	v_max_f32_e64 v138, |v21|, |v21|
	v_max_f32_e64 v139, |v20|, |v20|
	v_max_f32_e32 v138, v139, v138
	v_max3_f32 v135, v135, v137, v138
	s_waitcnt vmcnt(18)
	v_max_f32_e64 v137, |v11|, |v11|
	v_max_f32_e64 v138, |v10|, |v10|
	v_max_f32_e32 v137, v138, v137
	v_max_f32_e64 v138, |v13|, |v13|
	v_max_f32_e64 v139, |v12|, |v12|
	v_max_f32_e32 v138, v139, v138
	v_max3_f32 v135, v135, v137, v138
	s_waitcnt vmcnt(17)
	v_max_f32_e64 v137, |v7|, |v7|
	v_max_f32_e64 v138, |v6|, |v6|
	v_max_f32_e32 v137, v138, v137
	v_max_f32_e64 v138, |v9|, |v9|
	v_max_f32_e64 v139, |v8|, |v8|
	v_max_f32_e32 v138, v139, v138
	v_max3_f32 v135, v135, v137, v138
	s_waitcnt vmcnt(16)
; __device__ __forceinline__ void peer_row_store(const f32x4 (&v)[16], unsigned char* ws, int it, int layer, int lane) {
;     ...
;     float am = 0.f;
; #pragma unroll
;     for (int j = 0; j < 16; ++j) am = fmaxf(fmaxf(am, fmaxf(fabsf(v[j][0]), fabsf(v[j][1]))), fmaxf(fabsf(v[j][2]), fabsf(v[j][3])));
;     am = __uint_as_float(max64u(__float_as_uint(am)));
;     const float q = am > 0.f ? 256.0f / am : 0.f;
;     unsigned* dst = (unsigned*)(ws + (tbl ? WS_PV : WS_PU) + (size_t)r * D) + lane;
;     if (tbl) {
;         const int rl = it - NEXP;
;         unsigned char* pvl = ws + WS_PV + (size_t)layer * NEXP * D + (size_t)rl * 8 + (lane & 1) * 4;
;         unsigned char* pvg = ws + WS_PV + (size_t)layer * NEXP * D + (size_t)NEXP * 2048 + (size_t)rl * 2048 + 4 * lane;
; #pragma unroll
;         for (int j = 0; j < 16; ++j) { int w = __builtin_amdgcn_cvt_pk_bf8_f32(v[j][0] * q, v[j][1] * q, 0, false); w = __builtin_amdgcn_cvt_pk_bf8_f32(v[j][2] * q, v[j][3] * q, w, true);
;             if (j < 8) *(unsigned*)(pvl + (size_t)((lane >> 1) + 32 * j) * (NEXP * 8)) = (unsigned)w;
;             else *(unsigned*)(pvg + 256 * (j - 8)) = (unsigned)w; }
;     } else {
; #pragma unroll
;         for (int j = 0; j < 16; ++j) { int w = __builtin_amdgcn_cvt_pk_fp8_f32(v[j][0] * q, v[j][1] * q, 0, false); w = __builtin_amdgcn_cvt_pk_fp8_f32(v[j][2] * q, v[j][3] * q, w, true); dst[64 * j] = (unsigned)w; }
;     }
;     if (lane == 0) ((float*)(ws + (tbl ? WS_SV : WS_SU)))[r] = am * (1.0f / 256.0f);
	v_max_f32_e64 v137, |v3|, |v3|
	v_max_f32_e64 v138, |v2|, |v2|
	v_max_f32_e32 v137, v138, v137
	v_max_f32_e64 v138, |v5|, |v5|
	v_max_f32_e64 v139, |v4|, |v4|
	v_max_f32_e32 v138, v139, v138
	v_max3_f32 v135, v135, v137, v138
	s_ashr_i32 s11, s10, 31
	s_nop 0
	v_max_u32_dpp v135, v135, v135 quad_perm:[1,0,3,2] row_mask:0xf bank_mask:0xf bound_ctrl:1
	s_nop 1
	v_max_u32_dpp v135, v135, v135 quad_perm:[2,3,0,1] row_mask:0xf bank_mask:0xf bound_ctrl:1
	s_nop 1
	v_max_u32_dpp v135, v135, v135 row_half_mirror row_mask:0xf bank_mask:0xf bound_ctrl:1
	s_nop 1
	v_max_u32_dpp v135, v135, v135 row_mirror row_mask:0xf bank_mask:0xf bound_ctrl:1
	v_mov_b32_e32 v137, v135
	s_nop 1
	v_permlane16_swap_b32_e32 v135, v137
	v_max_u32_e32 v135, v135, v137
	v_mov_b32_e32 v137, v135
	s_nop 1
	v_permlane32_swap_b32_e32 v135, v137
	v_max_u32_e32 v135, v135, v137
	v_div_scale_f32 v137, s[12:13], v135, v135, s31
	v_rcp_f32_e32 v138, v137
	s_lshl_b64 s[12:13], s[10:11], 12
	v_fma_f32 v139, -v137, v138, 1.0
	v_fmac_f32_e32 v138, v139, v138
	v_div_scale_f32 v139, vcc, s31, v135, s31
	v_mul_f32_e32 v140, v139, v138
	v_fma_f32 v141, -v137, v140, v139
	v_fmac_f32_e32 v140, v141, v138
	v_fma_f32 v137, -v137, v140, v139
	v_div_fmas_f32 v137, v137, v138, v140
	v_div_fixup_f32 v137, v137, v135, s31
	v_cmp_lt_f32_e32 vcc, 0, v135
	v_mov_b32_e32 v140, v131
	v_lshl_add_u64 v[138:139], v[132:133], 0, s[12:13]
	v_cndmask_b32_e32 v137, 0, v137, vcc
	v_mul_f32_e32 v86, v86, v137
	v_mul_f32_e32 v87, v87, v137
	v_cvt_pk_fp8_f32 v140, v86, v87
	v_mul_f32_e32 v86, v88, v137
	v_mul_f32_e32 v62, v62, v137
	v_mul_f32_e32 v63, v63, v137
	v_mov_b32_e32 v88, v131
	v_cvt_pk_fp8_f32 v88, v62, v63
	v_mul_f32_e32 v62, v64, v137
	v_mul_f32_e32 v63, v65, v137
	v_mul_f32_e32 v50, v50, v137
	v_cvt_pk_fp8_f32 v88, v62, v63 op_sel:[0,0,1]
	v_mul_f32_e32 v51, v51, v137
	v_mov_b32_e32 v62, v131
	v_cvt_pk_fp8_f32 v62, v50, v51
	v_mul_f32_e32 v50, v52, v137
	v_mul_f32_e32 v51, v53, v137
	v_mul_f32_e32 v52, v54, v137
	v_mul_f32_e32 v53, v55, v137
	v_mov_b32_e32 v54, v131
	v_cvt_pk_fp8_f32 v54, v52, v53
	v_cvt_pk_fp8_f32 v62, v50, v51 op_sel:[0,0,1]
	v_mul_f32_e32 v50, v56, v137
	v_mul_f32_e32 v51, v57, v137
	v_cvt_pk_fp8_f32 v54, v50, v51 op_sel:[0,0,1]
	v_mul_f32_e32 v46, v46, v137
	v_mul_f32_e32 v47, v47, v137
	v_mov_b32_e32 v50, v131
	v_cvt_pk_fp8_f32 v50, v46, v47
	v_mul_f32_e32 v46, v48, v137
	v_mul_f32_e32 v42, v42, v137
	v_mul_f32_e32 v43, v43, v137
	v_mov_b32_e32 v48, v131
	v_cvt_pk_fp8_f32 v48, v42, v43
	v_mul_f32_e32 v42, v44, v137
	v_mul_f32_e32 v43, v45, v137
	v_mul_f32_e32 v38, v38, v137
	v_cvt_pk_fp8_f32 v48, v42, v43 op_sel:[0,0,1]
	v_mul_f32_e32 v39, v39, v137
	v_mov_b32_e32 v42, v131
	v_cvt_pk_fp8_f32 v42, v38, v39
	v_mul_f32_e32 v38, v40, v137
	v_mul_f32_e32 v34, v34, v137
	v_mul_f32_e32 v35, v35, v137
	v_mov_b32_e32 v40, v131
	v_cvt_pk_fp8_f32 v40, v34, v35
	v_mul_f32_e32 v34, v36, v137
	v_mul_f32_e32 v35, v37, v137
	v_mul_f32_e32 v30, v30, v137
	v_cvt_pk_fp8_f32 v40, v34, v35 op_sel:[0,0,1]
	v_mul_f32_e32 v31, v31, v137
	v_mov_b32_e32 v34, v131
	v_cvt_pk_fp8_f32 v34, v30, v31
	v_mul_f32_e32 v30, v32, v137
	v_mul_f32_e32 v26, v26, v137
	v_mul_f32_e32 v27, v27, v137
	v_mov_b32_e32 v32, v131
	v_cvt_pk_fp8_f32 v32, v26, v27
	v_mul_f32_e32 v26, v28, v137
	v_mul_f32_e32 v27, v29, v137
	v_mul_f32_e32 v22, v22, v137
	v_cvt_pk_fp8_f32 v32, v26, v27 op_sel:[0,0,1]
	v_mul_f32_e32 v23, v23, v137
	v_mov_b32_e32 v26, v131
	v_cvt_pk_fp8_f32 v26, v22, v23
	v_mul_f32_e32 v22, v24, v137
	v_mul_f32_e32 v14, v14, v137
	v_mul_f32_e32 v15, v15, v137
	v_mov_b32_e32 v24, v131
	v_cvt_pk_fp8_f32 v24, v14, v15
	v_mul_f32_e32 v15, v17, v137
	v_mul_f32_e32 v10, v10, v137
	v_mul_f32_e32 v11, v11, v137
	v_mov_b32_e32 v17, v131
	v_cvt_pk_fp8_f32 v17, v10, v11
	v_mul_f32_e32 v14, v16, v137
	v_cvt_pk_fp8_f32 v24, v14, v15 op_sel:[0,0,1]
	v_mul_f32_e32 v14, v18, v137
	v_mul_f32_e32 v15, v19, v137
	v_mov_b32_e32 v16, v131
	v_cvt_pk_fp8_f32 v16, v14, v15
	v_mul_f32_e32 v10, v12, v137
	v_mul_f32_e32 v11, v13, v137
	v_cvt_pk_fp8_f32 v17, v10, v11 op_sel:[0,0,1]
	v_mul_f32_e32 v6, v6, v137
	v_mul_f32_e32 v7, v7, v137
	v_mov_b32_e32 v10, v131
	v_cvt_pk_fp8_f32 v10, v6, v7
	v_mul_f32_e32 v6, v8, v137
	v_mul_f32_e32 v2, v2, v137
	v_mul_f32_e32 v3, v3, v137
	v_mov_b32_e32 v8, v131
	v_mul_f32_e32 v87, v89, v137
	v_mul_f32_e32 v47, v49, v137
	v_mul_f32_e32 v31, v33, v137
	v_mul_f32_e32 v14, v20, v137
	v_mul_f32_e32 v15, v21, v137
	v_cvt_pk_fp8_f32 v8, v2, v3
	v_cvt_pk_fp8_f32 v140, v86, v87 op_sel:[0,0,1]
	v_cvt_pk_fp8_f32 v50, v46, v47 op_sel:[0,0,1]
	v_cvt_pk_fp8_f32 v34, v30, v31 op_sel:[0,0,1]
	v_cvt_pk_fp8_f32 v16, v14, v15 op_sel:[0,0,1]
	v_mul_f32_e32 v39, v41, v137
	v_mul_f32_e32 v23, v25, v137
	v_mul_f32_e32 v7, v9, v137
	v_cvt_pk_fp8_f32 v42, v38, v39 op_sel:[0,0,1]
	v_cvt_pk_fp8_f32 v26, v22, v23 op_sel:[0,0,1]
	v_cvt_pk_fp8_f32 v10, v6, v7 op_sel:[0,0,1]
	v_mul_f32_e32 v2, v4, v137
	v_mul_f32_e32 v3, v5, v137
	v_cvt_pk_fp8_f32 v8, v2, v3 op_sel:[0,0,1]
	global_store_dword v[138:139], v140, off
	global_store_dword v[138:139], v88, off offset:256
	global_store_dword v[138:139], v62, off offset:512
	global_store_dword v[138:139], v54, off offset:768
	global_store_dword v[138:139], v50, off offset:1024
	global_store_dword v[138:139], v48, off offset:1280
	global_store_dword v[138:139], v42, off offset:1536
	global_store_dword v[138:139], v40, off offset:1792
	global_store_dword v[138:139], v34, off offset:2048
	global_store_dword v[138:139], v32, off offset:2304
	global_store_dword v[138:139], v26, off offset:2560
	global_store_dword v[138:139], v24, off offset:2816
	global_store_dword v[138:139], v16, off offset:3072
	global_store_dword v[138:139], v17, off offset:3328
	global_store_dword v[138:139], v10, off offset:3584
	global_store_dword v[138:139], v8, off offset:3840
	s_and_saveexec_b64 s[12:13], s[0:1]
	s_cbranch_execz .LBB0_624
	s_lshl_b64 s[20:21], s[10:11], 2
	s_add_u32 s20, s17, s20
	s_addc_u32 s21, s18, s21
	v_mul_f32_e32 v2, 0x3b800000, v135
	global_store_dword v131, v2, s[20:21]
; __device__ __forceinline__ void peer_row_store(const f32x4 (&v)[16], unsigned char* ws, int it, int layer, int lane) {
;     const int tbl = it >= NEXP, r = it - tbl * NEXP + layer * NEXP;
;     float am = 0.f;
; #pragma unroll
;     for (int j = 0; j < 16; ++j) am = fmaxf(fmaxf(am, fmaxf(fabsf(v[j][0]), fabsf(v[j][1]))), fmaxf(fabsf(v[j][2]), fabsf(v[j][3])));
;     am = __uint_as_float(max64u(__float_as_uint(am)));
;     ...
;         peer_row_load(va, in, it2 < it_hi ? it2 : it, only_layer, lane);
;         __builtin_amdgcn_sched_barrier(0);
;         if (it1 < it_hi) peer_row_store(vb, ws, it1, only_layer, lane);
.LBB0_624:
	s_or_b64 exec, exec, s[12:13]
	s_add_i32 s7, s29, s19
	s_cmpk_lt_i32 s7, 0x2800
	s_cselect_b32 s7, s7, s10
	s_cmpk_gt_i32 s7, 0x3fff
	s_cselect_b64 s[10:11], -1, 0
	s_and_b64 s[12:13], s[10:11], exec
	s_cselect_b32 s12, 0xffffc000, 0
	s_add_i32 s12, s12, s7
	s_and_b64 s[10:11], s[10:11], exec
	s_cselect_b32 s7, s87, s85
	s_cselect_b32 s20, s86, s84
	s_ashr_i32 s13, s12, 31
	s_lshl_b64 s[10:11], s[12:13], 14
	s_add_u32 s10, s20, s10
	s_addc_u32 s11, s7, s11
	v_lshl_add_u64 v[2:3], s[10:11], 0, v[130:131]
	v_add_co_u32_e32 v4, vcc, s5, v2
	global_load_dwordx4 v[62:65], v130, s[10:11] offset:1024
	global_load_dwordx4 v[50:53], v130, s[10:11] offset:2048
	v_addc_co_u32_e32 v5, vcc, 0, v3, vcc
	v_add_co_u32_e32 v6, vcc, s14, v2
	s_nop 1
	v_addc_co_u32_e32 v7, vcc, 0, v3, vcc
	global_load_dwordx4 v[54:57], v130, s[10:11] offset:3072
	global_load_dwordx4 v[46:49], v[6:7], off offset:-4096
	global_load_dwordx4 v[42:45], v[4:5], off offset:1024
	global_load_dwordx4 v[38:41], v[4:5], off offset:2048
	global_load_dwordx4 v[30:33], v[6:7], off
	global_load_dwordx4 v[26:29], v[6:7], off offset:1024
	global_load_dwordx4 v[22:25], v[6:7], off offset:2048
	global_load_dwordx4 v[14:17], v[6:7], off offset:3072
	v_add_co_u32_e32 v2, vcc, 0x3000, v2
	s_nop 1
	v_addc_co_u32_e32 v3, vcc, 0, v3, vcc
	global_load_dwordx4 v[34:37], v[4:5], off offset:3072
	global_load_dwordx4 v[18:21], v[2:3], off
	global_load_dwordx4 v[10:13], v[2:3], off offset:1024
	global_load_dwordx4 v[6:9], v[2:3], off offset:2048
	global_load_dwordx4 v[86:89], v130, s[10:11]
	s_nop 0
	global_load_dwordx4 v[2:5], v[2:3], off offset:3072
	s_andn2_b64 vcc, exec, s[8:9]
	s_cbranch_vccnz .LBB0_621
	s_waitcnt vmcnt(33)
	v_max_f32_e64 v130, |v127|, |v127|
	v_max_f32_e64 v135, |v126|, |v126|
	v_max_f32_e32 v130, v135, v130
	v_max_f32_e64 v135, |v129|, |v129|
	v_max_f32_e64 v137, |v128|, |v128|
	v_max_f32_e32 v135, v137, v135
	v_max3_f32 v130, v130, 0, v135
	v_max_f32_e64 v135, |v123|, |v123|
	v_max_f32_e64 v137, |v122|, |v122|
	v_max_f32_e32 v135, v137, v135
	v_max_f32_e64 v137, |v125|, |v125|
	v_max_f32_e64 v138, |v124|, |v124|
	v_max_f32_e32 v137, v138, v137
	v_max3_f32 v130, v130, v135, v137
	v_max_f32_e64 v135, |v119|, |v119|
	v_max_f32_e64 v137, |v118|, |v118|
	v_max_f32_e32 v135, v137, v135
	v_max_f32_e64 v137, |v121|, |v121|
	v_max_f32_e64 v138, |v120|, |v120|
	v_max_f32_e32 v137, v138, v137
	v_max3_f32 v130, v130, v135, v137
	v_max_f32_e64 v135, |v115|, |v115|
	v_max_f32_e64 v137, |v114|, |v114|
	v_max_f32_e32 v135, v137, v135
	v_max_f32_e64 v137, |v117|, |v117|
	v_max_f32_e64 v138, |v116|, |v116|
	v_max_f32_e32 v137, v138, v137
	v_max3_f32 v130, v130, v135, v137
	v_max_f32_e64 v135, |v111|, |v111|
	v_max_f32_e64 v137, |v110|, |v110|
	v_max_f32_e32 v135, v137, v135
	v_max_f32_e64 v137, |v113|, |v113|
	v_max_f32_e64 v138, |v112|, |v112|
	v_max_f32_e32 v137, v138, v137
	v_max3_f32 v130, v130, v135, v137
	v_max_f32_e64 v135, |v107|, |v107|
	v_max_f32_e64 v137, |v106|, |v106|
	v_max_f32_e32 v135, v137, v135
	v_max_f32_e64 v137, |v109|, |v109|
	v_max_f32_e64 v138, |v108|, |v108|
	v_max_f32_e32 v137, v138, v137
	v_max3_f32 v130, v130, v135, v137
	v_max_f32_e64 v135, |v103|, |v103|
	v_max_f32_e64 v137, |v102|, |v102|
	v_max_f32_e32 v135, v137, v135
	v_max_f32_e64 v137, |v105|, |v105|
	v_max_f32_e64 v138, |v104|, |v104|
	v_max_f32_e32 v137, v138, v137
	v_max3_f32 v130, v130, v135, v137
	v_max_f32_e64 v135, |v99|, |v99|
	v_max_f32_e64 v137, |v98|, |v98|
	v_max_f32_e32 v135, v137, v135
	v_max_f32_e64 v137, |v101|, |v101|
	v_max_f32_e64 v138, |v100|, |v100|
	v_max_f32_e32 v137, v138, v137
	v_max3_f32 v130, v130, v135, v137
	v_max_f32_e64 v135, |v95|, |v95|
	v_max_f32_e64 v137, |v94|, |v94|
	v_max_f32_e32 v135, v137, v135
	v_max_f32_e64 v137, |v97|, |v97|
	v_max_f32_e64 v138, |v96|, |v96|
	v_max_f32_e32 v137, v138, v137
	v_max3_f32 v130, v130, v135, v137
	v_max_f32_e64 v135, |v91|, |v91|
	v_max_f32_e64 v137, |v90|, |v90|
	v_max_f32_e32 v135, v137, v135
	v_max_f32_e64 v137, |v93|, |v93|
	v_max_f32_e64 v138, |v92|, |v92|
	v_max_f32_e32 v137, v138, v137
	v_max3_f32 v130, v130, v135, v137
	v_max_f32_e64 v135, |v83|, |v83|
	v_max_f32_e64 v137, |v82|, |v82|
	v_max_f32_e32 v135, v137, v135
	v_max_f32_e64 v137, |v85|, |v85|
	v_max_f32_e64 v138, |v84|, |v84|
	v_max_f32_e32 v137, v138, v137
	v_max3_f32 v130, v130, v135, v137
	v_max_f32_e64 v135, |v79|, |v79|
	v_max_f32_e64 v137, |v78|, |v78|
	v_max_f32_e32 v135, v137, v135
	v_max_f32_e64 v137, |v81|, |v81|
	v_max_f32_e64 v138, |v80|, |v80|
	v_max_f32_e32 v137, v138, v137
	v_max3_f32 v130, v130, v135, v137
	v_max_f32_e64 v135, |v75|, |v75|
	v_max_f32_e64 v137, |v74|, |v74|
	v_max_f32_e32 v135, v137, v135
	v_max_f32_e64 v137, |v77|, |v77|
	v_max_f32_e64 v138, |v76|, |v76|
	v_max_f32_e32 v137, v138, v137
	v_max3_f32 v130, v130, v135, v137
	v_max_f32_e64 v135, |v71|, |v71|
	v_max_f32_e64 v137, |v70|, |v70|
	v_max_f32_e32 v135, v137, v135
	v_max_f32_e64 v137, |v73|, |v73|
	v_max_f32_e64 v138, |v72|, |v72|
	v_max_f32_e32 v137, v138, v137
	v_max3_f32 v130, v130, v135, v137
	v_max_f32_e64 v135, |v67|, |v67|
	v_max_f32_e64 v137, |v66|, |v66|
	v_max_f32_e32 v135, v137, v135
	v_max_f32_e64 v137, |v69|, |v69|
	v_max_f32_e64 v138, |v68|, |v68|
	v_max_f32_e32 v137, v138, v137
	v_max3_f32 v130, v130, v135, v137
	s_waitcnt vmcnt(32)
; __device__ __forceinline__ void peer_row_store(const f32x4 (&v)[16], unsigned char* ws, int it, int layer, int lane) {
;     ...
;     float am = 0.f;
; #pragma unroll
;     for (int j = 0; j < 16; ++j) am = fmaxf(fmaxf(am, fmaxf(fabsf(v[j][0]), fabsf(v[j][1]))), fmaxf(fabsf(v[j][2]), fabsf(v[j][3])));
;     am = __uint_as_float(max64u(__float_as_uint(am)));
;     const float q = am > 0.f ? 256.0f / am : 0.f;
;     unsigned* dst = (unsigned*)(ws + (tbl ? WS_PV : WS_PU) + (size_t)r * D) + lane;
;     if (tbl) {
;         const int rl = it - NEXP;
;         unsigned char* pvl = ws + WS_PV + (size_t)layer * NEXP * D + (size_t)rl * 8 + (lane & 1) * 4;
;         unsigned char* pvg = ws + WS_PV + (size_t)layer * NEXP * D + (size_t)NEXP * 2048 + (size_t)rl * 2048 + 4 * lane;
; #pragma unroll
;         for (int j = 0; j < 16; ++j) { int w = __builtin_amdgcn_cvt_pk_bf8_f32(v[j][0] * q, v[j][1] * q, 0, false); w = __builtin_amdgcn_cvt_pk_bf8_f32(v[j][2] * q, v[j][3] * q, w, true);
;             if (j < 8) *(unsigned*)(pvl + (size_t)((lane >> 1) + 32 * j) * (NEXP * 8)) = (unsigned)w;
;             else *(unsigned*)(pvg + 256 * (j - 8)) = (unsigned)w; }
;     } else {
; #pragma unroll
;         for (int j = 0; j < 16; ++j) { int w = __builtin_amdgcn_cvt_pk_fp8_f32(v[j][0] * q, v[j][1] * q, 0, false); w = __builtin_amdgcn_cvt_pk_fp8_f32(v[j][2] * q, v[j][3] * q, w, true); dst[64 * j] = (unsigned)w; }
;     }
;     if (lane == 0) ((float*)(ws + (tbl ? WS_SV : WS_SU)))[r] = am * (1.0f / 256.0f);
	v_max_f32_e64 v135, |v59|, |v59|
	v_max_f32_e64 v137, |v58|, |v58|
	v_max_f32_e32 v135, v137, v135
	v_max_f32_e64 v137, |v61|, |v61|
	v_max_f32_e64 v138, |v60|, |v60|
	v_max_f32_e32 v137, v138, v137
	v_max3_f32 v130, v130, v135, v137
	s_ashr_i32 s7, s6, 31
	s_nop 0
	v_max_u32_dpp v130, v130, v130 quad_perm:[1,0,3,2] row_mask:0xf bank_mask:0xf bound_ctrl:1
	s_nop 1
	v_max_u32_dpp v130, v130, v130 quad_perm:[2,3,0,1] row_mask:0xf bank_mask:0xf bound_ctrl:1
	s_nop 1
	v_max_u32_dpp v130, v130, v130 row_half_mirror row_mask:0xf bank_mask:0xf bound_ctrl:1
	s_nop 1
	v_max_u32_dpp v130, v130, v130 row_mirror row_mask:0xf bank_mask:0xf bound_ctrl:1
	v_mov_b32_e32 v135, v130
	s_nop 1
	v_permlane16_swap_b32_e32 v130, v135
	v_max_u32_e32 v130, v130, v135
	v_mov_b32_e32 v135, v130
	s_nop 1
	v_permlane32_swap_b32_e32 v130, v135
	v_max_u32_e32 v130, v130, v135
	v_div_scale_f32 v135, s[8:9], v130, v130, s31
	v_rcp_f32_e32 v137, v135
	s_lshl_b64 s[8:9], s[6:7], 12
	v_fma_f32 v138, -v135, v137, 1.0
	v_fmac_f32_e32 v137, v138, v137
	v_div_scale_f32 v138, vcc, s31, v130, s31
	v_mul_f32_e32 v139, v138, v137
	v_fma_f32 v140, -v135, v139, v138
	v_fmac_f32_e32 v139, v140, v137
	v_fma_f32 v135, -v135, v139, v138
	v_div_fmas_f32 v135, v135, v137, v139
	v_div_fixup_f32 v135, v135, v130, s31
	v_cmp_lt_f32_e32 vcc, 0, v130
	v_mov_b32_e32 v137, v131
	v_lshl_add_u64 v[138:139], v[132:133], 0, s[8:9]
	v_cndmask_b32_e32 v135, 0, v135, vcc
	v_mul_f32_e32 v126, v126, v135
	v_mul_f32_e32 v127, v127, v135
	v_cvt_pk_fp8_f32 v137, v126, v127
	v_mul_f32_e32 v126, v128, v135
	v_mul_f32_e32 v122, v122, v135
	v_mul_f32_e32 v123, v123, v135
	v_mov_b32_e32 v128, v131
	v_cvt_pk_fp8_f32 v128, v122, v123
	v_mul_f32_e32 v122, v124, v135
	v_mul_f32_e32 v123, v125, v135
	v_mul_f32_e32 v118, v118, v135
	v_cvt_pk_fp8_f32 v128, v122, v123 op_sel:[0,0,1]
	v_mul_f32_e32 v119, v119, v135
	v_mov_b32_e32 v122, v131
	v_cvt_pk_fp8_f32 v122, v118, v119
	v_mul_f32_e32 v118, v120, v135
	v_mul_f32_e32 v114, v114, v135
	v_mul_f32_e32 v115, v115, v135
	v_mov_b32_e32 v120, v131
	v_cvt_pk_fp8_f32 v120, v114, v115
	v_mul_f32_e32 v114, v116, v135
	v_mul_f32_e32 v115, v117, v135
	v_mul_f32_e32 v110, v110, v135
	v_cvt_pk_fp8_f32 v120, v114, v115 op_sel:[0,0,1]
	v_mul_f32_e32 v111, v111, v135
	v_mov_b32_e32 v114, v131
	v_cvt_pk_fp8_f32 v114, v110, v111
	v_mul_f32_e32 v110, v112, v135
	v_mul_f32_e32 v106, v106, v135
	v_mul_f32_e32 v107, v107, v135
	v_mov_b32_e32 v112, v131
	v_cvt_pk_fp8_f32 v112, v106, v107
	v_mul_f32_e32 v106, v108, v135
	v_mul_f32_e32 v107, v109, v135
	v_mul_f32_e32 v102, v102, v135
	v_cvt_pk_fp8_f32 v112, v106, v107 op_sel:[0,0,1]
	v_mul_f32_e32 v103, v103, v135
	v_mov_b32_e32 v106, v131
	v_cvt_pk_fp8_f32 v106, v102, v103
	v_mul_f32_e32 v102, v104, v135
	v_mul_f32_e32 v98, v98, v135
	v_mul_f32_e32 v99, v99, v135
	v_mov_b32_e32 v104, v131
	v_cvt_pk_fp8_f32 v104, v98, v99
	v_mul_f32_e32 v98, v100, v135
	v_mul_f32_e32 v99, v101, v135
	v_mul_f32_e32 v94, v94, v135
	v_cvt_pk_fp8_f32 v104, v98, v99 op_sel:[0,0,1]
	v_mul_f32_e32 v95, v95, v135
	v_mov_b32_e32 v98, v131
	v_cvt_pk_fp8_f32 v98, v94, v95
	v_mul_f32_e32 v94, v96, v135
	v_mul_f32_e32 v90, v90, v135
	v_mul_f32_e32 v91, v91, v135
	v_mov_b32_e32 v96, v131
	v_cvt_pk_fp8_f32 v96, v90, v91
	v_mul_f32_e32 v90, v92, v135
	v_mul_f32_e32 v91, v93, v135
	v_mul_f32_e32 v82, v82, v135
	v_cvt_pk_fp8_f32 v96, v90, v91 op_sel:[0,0,1]
	v_mul_f32_e32 v83, v83, v135
	v_mov_b32_e32 v90, v131
	v_cvt_pk_fp8_f32 v90, v82, v83
	v_mul_f32_e32 v82, v84, v135
	v_mul_f32_e32 v78, v78, v135
	v_mul_f32_e32 v79, v79, v135
	v_mov_b32_e32 v84, v131
	v_cvt_pk_fp8_f32 v84, v78, v79
	v_mul_f32_e32 v78, v80, v135
	v_mul_f32_e32 v79, v81, v135
	v_mul_f32_e32 v74, v74, v135
	v_cvt_pk_fp8_f32 v84, v78, v79 op_sel:[0,0,1]
	v_mul_f32_e32 v75, v75, v135
	v_mov_b32_e32 v78, v131
	v_cvt_pk_fp8_f32 v78, v74, v75
	v_mul_f32_e32 v74, v76, v135
	v_mul_f32_e32 v70, v70, v135
	v_mul_f32_e32 v71, v71, v135
	v_mov_b32_e32 v76, v131
	v_cvt_pk_fp8_f32 v76, v70, v71
	v_mul_f32_e32 v70, v72, v135
	v_mul_f32_e32 v71, v73, v135
	v_mul_f32_e32 v66, v66, v135
	v_cvt_pk_fp8_f32 v76, v70, v71 op_sel:[0,0,1]
	v_mul_f32_e32 v67, v67, v135
	v_mov_b32_e32 v70, v131
	v_cvt_pk_fp8_f32 v70, v66, v67
	v_mul_f32_e32 v66, v68, v135
	v_mul_f32_e32 v58, v58, v135
	v_mul_f32_e32 v59, v59, v135
	v_mov_b32_e32 v68, v131
	v_mul_f32_e32 v127, v129, v135
	v_mul_f32_e32 v111, v113, v135
	v_mul_f32_e32 v95, v97, v135
	v_mul_f32_e32 v75, v77, v135
	v_cvt_pk_fp8_f32 v68, v58, v59
	v_cvt_pk_fp8_f32 v137, v126, v127 op_sel:[0,0,1]
	v_cvt_pk_fp8_f32 v114, v110, v111 op_sel:[0,0,1]
	v_cvt_pk_fp8_f32 v98, v94, v95 op_sel:[0,0,1]
	v_cvt_pk_fp8_f32 v78, v74, v75 op_sel:[0,0,1]
	v_mul_f32_e32 v119, v121, v135
	v_mul_f32_e32 v103, v105, v135
	v_mul_f32_e32 v83, v85, v135
	v_mul_f32_e32 v67, v69, v135
	v_cvt_pk_fp8_f32 v122, v118, v119 op_sel:[0,0,1]
	v_cvt_pk_fp8_f32 v106, v102, v103 op_sel:[0,0,1]
	v_cvt_pk_fp8_f32 v90, v82, v83 op_sel:[0,0,1]
	v_cvt_pk_fp8_f32 v70, v66, v67 op_sel:[0,0,1]
	v_mul_f32_e32 v58, v60, v135
	v_mul_f32_e32 v59, v61, v135
	v_cvt_pk_fp8_f32 v68, v58, v59 op_sel:[0,0,1]
	global_store_dword v[138:139], v137, off
	global_store_dword v[138:139], v128, off offset:256
	global_store_dword v[138:139], v122, off offset:512
	global_store_dword v[138:139], v120, off offset:768
	global_store_dword v[138:139], v114, off offset:1024
	global_store_dword v[138:139], v112, off offset:1280
	global_store_dword v[138:139], v106, off offset:1536
	global_store_dword v[138:139], v104, off offset:1792
	global_store_dword v[138:139], v98, off offset:2048
	global_store_dword v[138:139], v96, off offset:2304
	global_store_dword v[138:139], v90, off offset:2560
	global_store_dword v[138:139], v84, off offset:2816
	global_store_dword v[138:139], v78, off offset:3072
	global_store_dword v[138:139], v76, off offset:3328
	global_store_dword v[138:139], v70, off offset:3584
	global_store_dword v[138:139], v68, off offset:3840
	s_and_saveexec_b64 s[8:9], s[0:1]
	s_cbranch_execz .LBB0_620
	s_lshl_b64 s[6:7], s[6:7], 2
	s_add_u32 s6, s17, s6
	s_addc_u32 s7, s18, s7
	v_mul_f32_e32 v58, 0x3b800000, v130
	global_store_dword v131, v58, s[6:7]
	s_branch .LBB0_620

; __device__ __forceinline__ void peer_row_load(f32x4 (&v)[16], const float* const (&in)[34], int it, int layer, int lane) {
;     const int tbl = it >= NEXP, r = it - tbl * NEXP + layer * NEXP;
;     const f32x4* src = (const f32x4*)((tbl ? in[33] : in[32]) + (size_t)r * D) + lane;
; #pragma unroll
;     for (int j = 0; j < 16; ++j) v[j] = src[64 * j];
; }
; __device__ __forceinline__ void peer_row_store(const f32x4 (&v)[16], unsigned char* ws, int it, int layer, int lane) {
;     const int tbl = it >= NEXP, r = it - tbl * NEXP + layer * NEXP;
;     float am = 0.f;
; #pragma unroll
;     for (int j = 0; j < 16; ++j) am = fmaxf(fmaxf(am, fmaxf(fabsf(v[j][0]), fabsf(v[j][1]))), fmaxf(fabsf(v[j][2]), fabsf(v[j][3])));
;     am = __uint_as_float(max64u(__float_as_uint(am)));
;     const float q = am > 0.f ? 256.0f / am : 0.f;
;     unsigned* dst = (unsigned*)(ws + (tbl ? WS_PV : WS_PU) + (size_t)r * D) + lane;
;     if (tbl) {
;         const int rl = it - NEXP;
;         unsigned char* pvl = ws + WS_PV + (size_t)layer * NEXP * D + (size_t)rl * 8 + (lane & 1) * 4;
;         unsigned char* pvg = ws + WS_PV + (size_t)layer * NEXP * D + (size_t)NEXP * 2048 + (size_t)rl * 2048 + 4 * lane;
; #pragma unroll
;         for (int j = 0; j < 16; ++j) { int w = __builtin_amdgcn_cvt_pk_bf8_f32(v[j][0] * q, v[j][1] * q, 0, false); w = __builtin_amdgcn_cvt_pk_bf8_f32(v[j][2] * q, v[j][3] * q, w, true);
;             if (j < 8) *(unsigned*)(pvl + (size_t)((lane >> 1) + 32 * j) * (NEXP * 8)) = (unsigned)w;
;             else *(unsigned*)(pvg + 256 * (j - 8)) = (unsigned)w; }
;     } else {
; #pragma unroll
;         for (int j = 0; j < 16; ++j) { int w = __builtin_amdgcn_cvt_pk_fp8_f32(v[j][0] * q, v[j][1] * q, 0, false); w = __builtin_amdgcn_cvt_pk_fp8_f32(v[j][2] * q, v[j][3] * q, w, true); dst[64 * j] = (unsigned)w; }
;     }
;     if (lane == 0) ((float*)(ws + (tbl ? WS_SV : WS_SU)))[r] = am * (1.0f / 256.0f);
.Lp4r_conv:
	s_waitcnt vmcnt(0) lgkmcnt(0)
	v_and_b32_e32 v11, 63, v0
	v_lshrrev_b32_e32 v7, 6, v0
	v_lshlrev_b32_e32 v1, 4, v11
	v_readfirstlane_b32 s0, v7
	v_lshlrev_b32_e32 v2, 2, v11
	v_add_u32_e32 v3, 0x1000, v1
	v_add_u32_e32 v4, 0x2000, v1
	v_add_u32_e32 v5, 0x3000, v1
	v_mov_b32_e32 v10, 0
	v_cmp_eq_u32_e64 s[12:13], 0, v11
	s_lshl_b32 s1, s2, 3
	s_add_i32 s4, s1, s0
	s_addk_i32 s4, 0x2800
	s_mov_b32 s14, 0x43800000
	s_lshl_b32 s1, s4, 14
	s_add_u32 s6, s84, s1
	s_addc_u32 s7, s85, 0
	global_load_dwordx4 v[40:43], v1, s[6:7]
	global_load_dwordx4 v[44:47], v1, s[6:7] offset:1024
	global_load_dwordx4 v[48:51], v1, s[6:7] offset:2048
	global_load_dwordx4 v[52:55], v1, s[6:7] offset:3072
	global_load_dwordx4 v[56:59], v3, s[6:7]
	global_load_dwordx4 v[60:63], v3, s[6:7] offset:1024
	global_load_dwordx4 v[64:67], v3, s[6:7] offset:2048
	global_load_dwordx4 v[68:71], v3, s[6:7] offset:3072
	global_load_dwordx4 v[72:75], v4, s[6:7]
	global_load_dwordx4 v[76:79], v4, s[6:7] offset:1024
	global_load_dwordx4 v[80:83], v4, s[6:7] offset:2048
	global_load_dwordx4 v[84:87], v4, s[6:7] offset:3072
	global_load_dwordx4 v[88:91], v5, s[6:7]
	global_load_dwordx4 v[92:95], v5, s[6:7] offset:1024
	global_load_dwordx4 v[96:99], v5, s[6:7] offset:2048
	global_load_dwordx4 v[100:103], v5, s[6:7] offset:3072
	s_add_i32 s5, s4, 1024
	s_lshl_b32 s1, s5, 14
	s_add_u32 s6, s84, s1
	s_addc_u32 s7, s85, 0
	global_load_dwordx4 v[104:107], v1, s[6:7]
	global_load_dwordx4 v[108:111], v1, s[6:7] offset:1024
	global_load_dwordx4 v[112:115], v1, s[6:7] offset:2048
	global_load_dwordx4 v[116:119], v1, s[6:7] offset:3072
	global_load_dwordx4 v[120:123], v3, s[6:7]
	global_load_dwordx4 v[124:127], v3, s[6:7] offset:1024
	global_load_dwordx4 v[128:131], v3, s[6:7] offset:2048
	global_load_dwordx4 v[132:135], v3, s[6:7] offset:3072
	global_load_dwordx4 v[136:139], v4, s[6:7]
	global_load_dwordx4 v[140:143], v4, s[6:7] offset:1024
	global_load_dwordx4 v[144:147], v4, s[6:7] offset:2048
	global_load_dwordx4 v[148:151], v4, s[6:7] offset:3072
	global_load_dwordx4 v[152:155], v5, s[6:7]
	global_load_dwordx4 v[156:159], v5, s[6:7] offset:1024
	global_load_dwordx4 v[160:163], v5, s[6:7] offset:2048
	global_load_dwordx4 v[164:167], v5, s[6:7] offset:3072
	s_waitcnt vmcnt(31)
	v_max3_f32 v6, |v40|, |v41|, 0
	v_max3_f32 v6, |v42|, |v43|, v6
	s_waitcnt vmcnt(30)
	v_max3_f32 v6, |v44|, |v45|, v6
	v_max3_f32 v6, |v46|, |v47|, v6
	s_waitcnt vmcnt(29)
	v_max3_f32 v6, |v48|, |v49|, v6
	v_max3_f32 v6, |v50|, |v51|, v6
	s_waitcnt vmcnt(28)
	v_max3_f32 v6, |v52|, |v53|, v6
	v_max3_f32 v6, |v54|, |v55|, v6
	s_waitcnt vmcnt(27)
	v_max3_f32 v6, |v56|, |v57|, v6
	v_max3_f32 v6, |v58|, |v59|, v6
	s_waitcnt vmcnt(26)
	v_max3_f32 v6, |v60|, |v61|, v6
	v_max3_f32 v6, |v62|, |v63|, v6
	s_waitcnt vmcnt(25)
	v_max3_f32 v6, |v64|, |v65|, v6
	v_max3_f32 v6, |v66|, |v67|, v6
	s_waitcnt vmcnt(24)
	v_max3_f32 v6, |v68|, |v69|, v6
	v_max3_f32 v6, |v70|, |v71|, v6
	s_waitcnt vmcnt(23)
	v_max3_f32 v6, |v72|, |v73|, v6
	v_max3_f32 v6, |v74|, |v75|, v6
	s_waitcnt vmcnt(22)
	v_max3_f32 v6, |v76|, |v77|, v6
	v_max3_f32 v6, |v78|, |v79|, v6
	s_waitcnt vmcnt(21)
	v_max3_f32 v6, |v80|, |v81|, v6
	v_max3_f32 v6, |v82|, |v83|, v6
	s_waitcnt vmcnt(20)
	v_max3_f32 v6, |v84|, |v85|, v6
	v_max3_f32 v6, |v86|, |v87|, v6
	s_waitcnt vmcnt(19)
	v_max3_f32 v6, |v88|, |v89|, v6
	v_max3_f32 v6, |v90|, |v91|, v6
	s_waitcnt vmcnt(18)
	v_max3_f32 v6, |v92|, |v93|, v6
	v_max3_f32 v6, |v94|, |v95|, v6
	s_waitcnt vmcnt(17)
	v_max3_f32 v6, |v96|, |v97|, v6
	v_max3_f32 v6, |v98|, |v99|, v6
	s_waitcnt vmcnt(16)
	v_max3_f32 v6, |v100|, |v101|, v6
	v_max3_f32 v6, |v102|, |v103|, v6
	s_nop 1
	v_max_u32_dpp v6, v6, v6 quad_perm:[1,0,3,2] row_mask:0xf bank_mask:0xf bound_ctrl:1
	s_nop 1
	v_max_u32_dpp v6, v6, v6 quad_perm:[2,3,0,1] row_mask:0xf bank_mask:0xf bound_ctrl:1
	s_nop 1
	v_max_u32_dpp v6, v6, v6 row_half_mirror row_mask:0xf bank_mask:0xf bound_ctrl:1
	s_nop 1
	v_max_u32_dpp v6, v6, v6 row_mirror row_mask:0xf bank_mask:0xf bound_ctrl:1
	s_nop 1
	v_mov_b32_e32 v7, v6
	s_nop 1
	v_permlane16_swap_b32_e32 v6, v7
	v_max_u32_e32 v6, v6, v7
	v_mov_b32_e32 v7, v6
	s_nop 1
	v_permlane32_swap_b32_e32 v6, v7
	v_max_u32_e32 v6, v6, v7
	v_div_scale_f32 v12, s[16:17], v6, v6, s14
	v_rcp_f32_e32 v13, v12
	s_nop 0
	v_fma_f32 v14, -v12, v13, 1.0
	v_fmac_f32_e32 v13, v14, v13
	v_div_scale_f32 v14, vcc, s14, v6, s14
	v_mul_f32_e32 v15, v14, v13
	v_fma_f32 v16, -v12, v15, v14
	v_fmac_f32_e32 v15, v16, v13
	v_fma_f32 v12, -v12, v15, v14
	v_div_fmas_f32 v12, v12, v13, v15
	v_div_fixup_f32 v9, v12, v6, s14
	v_cmp_lt_f32_e32 vcc, 0, v6
	s_nop 1
	v_cndmask_b32_e32 v9, 0, v9, vcc
	s_lshl_b32 s1, s4, 12
	s_add_u32 s8, s90, 0xba00000
	s_addc_u32 s9, s91, 0
	s_add_u32 s8, s8, s1
	s_addc_u32 s9, s9, 0
	s_lshl_b32 s1, s4, 2
	s_add_u32 s10, s90, 0x1ba00000
	s_addc_u32 s11, s91, 0
	s_add_u32 s10, s10, s1
	s_addc_u32 s11, s11, 0
	v_mul_f32_e32 v40, v40, v9
	v_mul_f32_e32 v41, v41, v9
	v_mul_f32_e32 v42, v42, v9
	v_mul_f32_e32 v43, v43, v9
	v_mov_b32_e32 v20, v10
	v_cvt_pk_fp8_f32 v20, v40, v41
	v_mul_f32_e32 v44, v44, v9
	v_mul_f32_e32 v45, v45, v9
	v_mul_f32_e32 v46, v46, v9
	v_mul_f32_e32 v47, v47, v9
	v_mov_b32_e32 v21, v10
	v_cvt_pk_fp8_f32 v21, v44, v45
	v_cvt_pk_fp8_f32 v20, v42, v43 op_sel:[0,0,1]
	v_mul_f32_e32 v48, v48, v9
	v_mul_f32_e32 v49, v49, v9
	v_mul_f32_e32 v50, v50, v9
	v_mul_f32_e32 v51, v51, v9
	v_mov_b32_e32 v22, v10
	v_cvt_pk_fp8_f32 v22, v48, v49
	v_cvt_pk_fp8_f32 v21, v46, v47 op_sel:[0,0,1]
	v_mul_f32_e32 v52, v52, v9
	v_mul_f32_e32 v53, v53, v9
	v_mul_f32_e32 v54, v54, v9
	v_mul_f32_e32 v55, v55, v9
	v_mov_b32_e32 v23, v10
; __device__ __forceinline__ void peer_row_load(f32x4 (&v)[16], const float* const (&in)[34], int it, int layer, int lane) {
;     const int tbl = it >= NEXP, r = it - tbl * NEXP + layer * NEXP;
;     const f32x4* src = (const f32x4*)((tbl ? in[33] : in[32]) + (size_t)r * D) + lane;
; #pragma unroll
;     for (int j = 0; j < 16; ++j) v[j] = src[64 * j];
; }
; __device__ __forceinline__ void peer_row_store(const f32x4 (&v)[16], unsigned char* ws, int it, int layer, int lane) {
;     const int tbl = it >= NEXP, r = it - tbl * NEXP + layer * NEXP;
;     float am = 0.f;
; #pragma unroll
;     for (int j = 0; j < 16; ++j) am = fmaxf(fmaxf(am, fmaxf(fabsf(v[j][0]), fabsf(v[j][1]))), fmaxf(fabsf(v[j][2]), fabsf(v[j][3])));
;     am = __uint_as_float(max64u(__float_as_uint(am)));
;     const float q = am > 0.f ? 256.0f / am : 0.f;
;     unsigned* dst = (unsigned*)(ws + (tbl ? WS_PV : WS_PU) + (size_t)r * D) + lane;
;     if (tbl) {
;         const int rl = it - NEXP;
;         unsigned char* pvl = ws + WS_PV + (size_t)layer * NEXP * D + (size_t)rl * 8 + (lane & 1) * 4;
;         unsigned char* pvg = ws + WS_PV + (size_t)layer * NEXP * D + (size_t)NEXP * 2048 + (size_t)rl * 2048 + 4 * lane;
; #pragma unroll
;         for (int j = 0; j < 16; ++j) { int w = __builtin_amdgcn_cvt_pk_bf8_f32(v[j][0] * q, v[j][1] * q, 0, false); w = __builtin_amdgcn_cvt_pk_bf8_f32(v[j][2] * q, v[j][3] * q, w, true);
;             if (j < 8) *(unsigned*)(pvl + (size_t)((lane >> 1) + 32 * j) * (NEXP * 8)) = (unsigned)w;
;             else *(unsigned*)(pvg + 256 * (j - 8)) = (unsigned)w; }
;     } else {
; #pragma unroll
;         for (int j = 0; j < 16; ++j) { int w = __builtin_amdgcn_cvt_pk_fp8_f32(v[j][0] * q, v[j][1] * q, 0, false); w = __builtin_amdgcn_cvt_pk_fp8_f32(v[j][2] * q, v[j][3] * q, w, true); dst[64 * j] = (unsigned)w; }
;     }
;     if (lane == 0) ((float*)(ws + (tbl ? WS_SV : WS_SU)))[r] = am * (1.0f / 256.0f);
	v_cvt_pk_fp8_f32 v23, v52, v53
	v_cvt_pk_fp8_f32 v22, v50, v51 op_sel:[0,0,1]
	v_mul_f32_e32 v56, v56, v9
	v_mul_f32_e32 v57, v57, v9
	v_mul_f32_e32 v58, v58, v9
	v_mul_f32_e32 v59, v59, v9
	v_mov_b32_e32 v24, v10
	v_cvt_pk_fp8_f32 v24, v56, v57
	v_cvt_pk_fp8_f32 v23, v54, v55 op_sel:[0,0,1]
	v_mul_f32_e32 v60, v60, v9
	v_mul_f32_e32 v61, v61, v9
	v_mul_f32_e32 v62, v62, v9
	v_mul_f32_e32 v63, v63, v9
	v_mov_b32_e32 v25, v10
	v_cvt_pk_fp8_f32 v25, v60, v61
	v_cvt_pk_fp8_f32 v24, v58, v59 op_sel:[0,0,1]
	v_mul_f32_e32 v64, v64, v9
	v_mul_f32_e32 v65, v65, v9
	v_mul_f32_e32 v66, v66, v9
	v_mul_f32_e32 v67, v67, v9
	v_mov_b32_e32 v26, v10
	v_cvt_pk_fp8_f32 v26, v64, v65
	v_cvt_pk_fp8_f32 v25, v62, v63 op_sel:[0,0,1]
	v_mul_f32_e32 v68, v68, v9
	v_mul_f32_e32 v69, v69, v9
	v_mul_f32_e32 v70, v70, v9
	v_mul_f32_e32 v71, v71, v9
	v_mov_b32_e32 v27, v10
	v_cvt_pk_fp8_f32 v27, v68, v69
	v_cvt_pk_fp8_f32 v26, v66, v67 op_sel:[0,0,1]
	v_mul_f32_e32 v72, v72, v9
	v_mul_f32_e32 v73, v73, v9
	v_mul_f32_e32 v74, v74, v9
	v_mul_f32_e32 v75, v75, v9
	v_mov_b32_e32 v28, v10
	v_cvt_pk_fp8_f32 v28, v72, v73
	v_cvt_pk_fp8_f32 v27, v70, v71 op_sel:[0,0,1]
	v_mul_f32_e32 v76, v76, v9
	v_mul_f32_e32 v77, v77, v9
	v_mul_f32_e32 v78, v78, v9
	v_mul_f32_e32 v79, v79, v9
	v_mov_b32_e32 v29, v10
	v_cvt_pk_fp8_f32 v29, v76, v77
	v_cvt_pk_fp8_f32 v28, v74, v75 op_sel:[0,0,1]
	v_mul_f32_e32 v80, v80, v9
	v_mul_f32_e32 v81, v81, v9
	v_mul_f32_e32 v82, v82, v9
	v_mul_f32_e32 v83, v83, v9
	v_mov_b32_e32 v30, v10
	v_cvt_pk_fp8_f32 v30, v80, v81
	v_cvt_pk_fp8_f32 v29, v78, v79 op_sel:[0,0,1]
	v_mul_f32_e32 v84, v84, v9
	v_mul_f32_e32 v85, v85, v9
	v_mul_f32_e32 v86, v86, v9
	v_mul_f32_e32 v87, v87, v9
	v_mov_b32_e32 v31, v10
	v_cvt_pk_fp8_f32 v31, v84, v85
	v_cvt_pk_fp8_f32 v30, v82, v83 op_sel:[0,0,1]
	v_mul_f32_e32 v88, v88, v9
	v_mul_f32_e32 v89, v89, v9
	v_mul_f32_e32 v90, v90, v9
	v_mul_f32_e32 v91, v91, v9
	v_mov_b32_e32 v32, v10
	v_cvt_pk_fp8_f32 v32, v88, v89
	v_cvt_pk_fp8_f32 v31, v86, v87 op_sel:[0,0,1]
	v_mul_f32_e32 v92, v92, v9
	v_mul_f32_e32 v93, v93, v9
	v_mul_f32_e32 v94, v94, v9
	v_mul_f32_e32 v95, v95, v9
	v_mov_b32_e32 v33, v10
	v_cvt_pk_fp8_f32 v33, v92, v93
	v_cvt_pk_fp8_f32 v32, v90, v91 op_sel:[0,0,1]
	v_mul_f32_e32 v96, v96, v9
	v_mul_f32_e32 v97, v97, v9
	v_mul_f32_e32 v98, v98, v9
	v_mul_f32_e32 v99, v99, v9
	v_mov_b32_e32 v34, v10
	v_cvt_pk_fp8_f32 v34, v96, v97
	v_cvt_pk_fp8_f32 v33, v94, v95 op_sel:[0,0,1]
	v_mul_f32_e32 v100, v100, v9
	v_mul_f32_e32 v101, v101, v9
	v_mul_f32_e32 v102, v102, v9
	v_mul_f32_e32 v103, v103, v9
	v_mov_b32_e32 v35, v10
	v_cvt_pk_fp8_f32 v35, v100, v101
	v_cvt_pk_fp8_f32 v34, v98, v99 op_sel:[0,0,1]
	v_cvt_pk_fp8_f32 v35, v102, v103 op_sel:[0,0,1]
	s_nop 0
	v_mul_f32_e32 v8, 0x3b800000, v6
	global_store_dword v2, v20, s[8:9]
	global_store_dword v2, v21, s[8:9] offset:256
	global_store_dword v2, v22, s[8:9] offset:512
	global_store_dword v2, v23, s[8:9] offset:768
	global_store_dword v2, v24, s[8:9] offset:1024
	global_store_dword v2, v25, s[8:9] offset:1280
	global_store_dword v2, v26, s[8:9] offset:1536
	global_store_dword v2, v27, s[8:9] offset:1792
	global_store_dword v2, v28, s[8:9] offset:2048
	global_store_dword v2, v29, s[8:9] offset:2304
	global_store_dword v2, v30, s[8:9] offset:2560
	global_store_dword v2, v31, s[8:9] offset:2816
	global_store_dword v2, v32, s[8:9] offset:3072
	global_store_dword v2, v33, s[8:9] offset:3328
	global_store_dword v2, v34, s[8:9] offset:3584
	global_store_dword v2, v35, s[8:9] offset:3840
	s_mov_b64 s[18:19], exec
	s_mov_b64 exec, s[12:13]
	global_store_dword v10, v8, s[10:11]
	s_mov_b64 exec, s[18:19]
	s_mov_b32 s4, s5
	s_add_i32 s5, s4, 1024
	s_lshl_b32 s1, s5, 14
	s_add_u32 s6, s84, s1
	s_addc_u32 s7, s85, 0
	global_load_dwordx4 v[40:43], v1, s[6:7]
	global_load_dwordx4 v[44:47], v1, s[6:7] offset:1024
	global_load_dwordx4 v[48:51], v1, s[6:7] offset:2048
	global_load_dwordx4 v[52:55], v1, s[6:7] offset:3072
	global_load_dwordx4 v[56:59], v3, s[6:7]
	global_load_dwordx4 v[60:63], v3, s[6:7] offset:1024
	global_load_dwordx4 v[64:67], v3, s[6:7] offset:2048
	global_load_dwordx4 v[68:71], v3, s[6:7] offset:3072
	global_load_dwordx4 v[72:75], v4, s[6:7]
	global_load_dwordx4 v[76:79], v4, s[6:7] offset:1024
	global_load_dwordx4 v[80:83], v4, s[6:7] offset:2048
	global_load_dwordx4 v[84:87], v4, s[6:7] offset:3072
	global_load_dwordx4 v[88:91], v5, s[6:7]
	global_load_dwordx4 v[92:95], v5, s[6:7] offset:1024
	global_load_dwordx4 v[96:99], v5, s[6:7] offset:2048
	global_load_dwordx4 v[100:103], v5, s[6:7] offset:3072
	s_waitcnt vmcnt(48)
	v_max3_f32 v6, |v104|, |v105|, 0
	v_max3_f32 v6, |v106|, |v107|, v6
	s_waitcnt vmcnt(47)
	v_max3_f32 v6, |v108|, |v109|, v6
	v_max3_f32 v6, |v110|, |v111|, v6
	s_waitcnt vmcnt(46)
	v_max3_f32 v6, |v112|, |v113|, v6
	v_max3_f32 v6, |v114|, |v115|, v6
	s_waitcnt vmcnt(45)
	v_max3_f32 v6, |v116|, |v117|, v6
	v_max3_f32 v6, |v118|, |v119|, v6
	s_waitcnt vmcnt(44)
	v_max3_f32 v6, |v120|, |v121|, v6
	v_max3_f32 v6, |v122|, |v123|, v6
	s_waitcnt vmcnt(43)
	v_max3_f32 v6, |v124|, |v125|, v6
	v_max3_f32 v6, |v126|, |v127|, v6
	s_waitcnt vmcnt(42)
	v_max3_f32 v6, |v128|, |v129|, v6
	v_max3_f32 v6, |v130|, |v131|, v6
	s_waitcnt vmcnt(41)
	v_max3_f32 v6, |v132|, |v133|, v6
	v_max3_f32 v6, |v134|, |v135|, v6
	s_waitcnt vmcnt(40)
	v_max3_f32 v6, |v136|, |v137|, v6
	v_max3_f32 v6, |v138|, |v139|, v6
	s_waitcnt vmcnt(39)
	v_max3_f32 v6, |v140|, |v141|, v6
	v_max3_f32 v6, |v142|, |v143|, v6
	s_waitcnt vmcnt(38)
	v_max3_f32 v6, |v144|, |v145|, v6
	v_max3_f32 v6, |v146|, |v147|, v6
	s_waitcnt vmcnt(37)
	v_max3_f32 v6, |v148|, |v149|, v6
	v_max3_f32 v6, |v150|, |v151|, v6
	s_waitcnt vmcnt(36)
; __device__ __forceinline__ void peer_row_load(f32x4 (&v)[16], const float* const (&in)[34], int it, int layer, int lane) {
;     const int tbl = it >= NEXP, r = it - tbl * NEXP + layer * NEXP;
;     const f32x4* src = (const f32x4*)((tbl ? in[33] : in[32]) + (size_t)r * D) + lane;
; #pragma unroll
;     for (int j = 0; j < 16; ++j) v[j] = src[64 * j];
; }
; __device__ __forceinline__ void peer_row_store(const f32x4 (&v)[16], unsigned char* ws, int it, int layer, int lane) {
;     const int tbl = it >= NEXP, r = it - tbl * NEXP + layer * NEXP;
;     float am = 0.f;
; #pragma unroll
;     for (int j = 0; j < 16; ++j) am = fmaxf(fmaxf(am, fmaxf(fabsf(v[j][0]), fabsf(v[j][1]))), fmaxf(fabsf(v[j][2]), fabsf(v[j][3])));
;     am = __uint_as_float(max64u(__float_as_uint(am)));
;     const float q = am > 0.f ? 256.0f / am : 0.f;
;     unsigned* dst = (unsigned*)(ws + (tbl ? WS_PV : WS_PU) + (size_t)r * D) + lane;
;     if (tbl) {
;         const int rl = it - NEXP;
;         unsigned char* pvl = ws + WS_PV + (size_t)layer * NEXP * D + (size_t)rl * 8 + (lane & 1) * 4;
;         unsigned char* pvg = ws + WS_PV + (size_t)layer * NEXP * D + (size_t)NEXP * 2048 + (size_t)rl * 2048 + 4 * lane;
; #pragma unroll
;         for (int j = 0; j < 16; ++j) { int w = __builtin_amdgcn_cvt_pk_bf8_f32(v[j][0] * q, v[j][1] * q, 0, false); w = __builtin_amdgcn_cvt_pk_bf8_f32(v[j][2] * q, v[j][3] * q, w, true);
;             if (j < 8) *(unsigned*)(pvl + (size_t)((lane >> 1) + 32 * j) * (NEXP * 8)) = (unsigned)w;
;             else *(unsigned*)(pvg + 256 * (j - 8)) = (unsigned)w; }
;     } else {
; #pragma unroll
;         for (int j = 0; j < 16; ++j) { int w = __builtin_amdgcn_cvt_pk_fp8_f32(v[j][0] * q, v[j][1] * q, 0, false); w = __builtin_amdgcn_cvt_pk_fp8_f32(v[j][2] * q, v[j][3] * q, w, true); dst[64 * j] = (unsigned)w; }
;     }
;     if (lane == 0) ((float*)(ws + (tbl ? WS_SV : WS_SU)))[r] = am * (1.0f / 256.0f);
	v_max3_f32 v6, |v152|, |v153|, v6
	v_max3_f32 v6, |v154|, |v155|, v6
	s_waitcnt vmcnt(35)
	v_max3_f32 v6, |v156|, |v157|, v6
	v_max3_f32 v6, |v158|, |v159|, v6
	s_waitcnt vmcnt(34)
	v_max3_f32 v6, |v160|, |v161|, v6
	v_max3_f32 v6, |v162|, |v163|, v6
	s_waitcnt vmcnt(33)
	v_max3_f32 v6, |v164|, |v165|, v6
	v_max3_f32 v6, |v166|, |v167|, v6
	s_nop 1
	v_max_u32_dpp v6, v6, v6 quad_perm:[1,0,3,2] row_mask:0xf bank_mask:0xf bound_ctrl:1
	s_nop 1
	v_max_u32_dpp v6, v6, v6 quad_perm:[2,3,0,1] row_mask:0xf bank_mask:0xf bound_ctrl:1
	s_nop 1
	v_max_u32_dpp v6, v6, v6 row_half_mirror row_mask:0xf bank_mask:0xf bound_ctrl:1
	s_nop 1
	v_max_u32_dpp v6, v6, v6 row_mirror row_mask:0xf bank_mask:0xf bound_ctrl:1
	s_nop 1
	v_mov_b32_e32 v7, v6
	s_nop 1
	v_permlane16_swap_b32_e32 v6, v7
	v_max_u32_e32 v6, v6, v7
	v_mov_b32_e32 v7, v6
	s_nop 1
	v_permlane32_swap_b32_e32 v6, v7
	v_max_u32_e32 v6, v6, v7
	v_div_scale_f32 v12, s[16:17], v6, v6, s14
	v_rcp_f32_e32 v13, v12
	s_nop 0
	v_fma_f32 v14, -v12, v13, 1.0
	v_fmac_f32_e32 v13, v14, v13
	v_div_scale_f32 v14, vcc, s14, v6, s14
	v_mul_f32_e32 v15, v14, v13
	v_fma_f32 v16, -v12, v15, v14
	v_fmac_f32_e32 v15, v16, v13
	v_fma_f32 v12, -v12, v15, v14
	v_div_fmas_f32 v12, v12, v13, v15
	v_div_fixup_f32 v9, v12, v6, s14
	v_cmp_lt_f32_e32 vcc, 0, v6
	s_nop 1
	v_cndmask_b32_e32 v9, 0, v9, vcc
	s_lshl_b32 s1, s4, 12
	s_add_u32 s8, s90, 0xba00000
	s_addc_u32 s9, s91, 0
	s_add_u32 s8, s8, s1
	s_addc_u32 s9, s9, 0
	s_lshl_b32 s1, s4, 2
	s_add_u32 s10, s90, 0x1ba00000
	s_addc_u32 s11, s91, 0
	s_add_u32 s10, s10, s1
	s_addc_u32 s11, s11, 0
	v_mul_f32_e32 v104, v104, v9
	v_mul_f32_e32 v105, v105, v9
	v_mul_f32_e32 v106, v106, v9
	v_mul_f32_e32 v107, v107, v9
	v_mov_b32_e32 v20, v10
	v_cvt_pk_fp8_f32 v20, v104, v105
	v_mul_f32_e32 v108, v108, v9
	v_mul_f32_e32 v109, v109, v9
	v_mul_f32_e32 v110, v110, v9
	v_mul_f32_e32 v111, v111, v9
	v_mov_b32_e32 v21, v10
	v_cvt_pk_fp8_f32 v21, v108, v109
	v_cvt_pk_fp8_f32 v20, v106, v107 op_sel:[0,0,1]
	v_mul_f32_e32 v112, v112, v9
	v_mul_f32_e32 v113, v113, v9
	v_mul_f32_e32 v114, v114, v9
	v_mul_f32_e32 v115, v115, v9
	v_mov_b32_e32 v22, v10
	v_cvt_pk_fp8_f32 v22, v112, v113
	v_cvt_pk_fp8_f32 v21, v110, v111 op_sel:[0,0,1]
	v_mul_f32_e32 v116, v116, v9
	v_mul_f32_e32 v117, v117, v9
	v_mul_f32_e32 v118, v118, v9
	v_mul_f32_e32 v119, v119, v9
	v_mov_b32_e32 v23, v10
	v_cvt_pk_fp8_f32 v23, v116, v117
	v_cvt_pk_fp8_f32 v22, v114, v115 op_sel:[0,0,1]
	v_mul_f32_e32 v120, v120, v9
	v_mul_f32_e32 v121, v121, v9
	v_mul_f32_e32 v122, v122, v9
	v_mul_f32_e32 v123, v123, v9
	v_mov_b32_e32 v24, v10
	v_cvt_pk_fp8_f32 v24, v120, v121
	v_cvt_pk_fp8_f32 v23, v118, v119 op_sel:[0,0,1]
	v_mul_f32_e32 v124, v124, v9
	v_mul_f32_e32 v125, v125, v9
	v_mul_f32_e32 v126, v126, v9
	v_mul_f32_e32 v127, v127, v9
	v_mov_b32_e32 v25, v10
	v_cvt_pk_fp8_f32 v25, v124, v125
	v_cvt_pk_fp8_f32 v24, v122, v123 op_sel:[0,0,1]
	v_mul_f32_e32 v128, v128, v9
	v_mul_f32_e32 v129, v129, v9
	v_mul_f32_e32 v130, v130, v9
	v_mul_f32_e32 v131, v131, v9
	v_mov_b32_e32 v26, v10
	v_cvt_pk_fp8_f32 v26, v128, v129
	v_cvt_pk_fp8_f32 v25, v126, v127 op_sel:[0,0,1]
	v_mul_f32_e32 v132, v132, v9
	v_mul_f32_e32 v133, v133, v9
	v_mul_f32_e32 v134, v134, v9
	v_mul_f32_e32 v135, v135, v9
	v_mov_b32_e32 v27, v10
	v_cvt_pk_fp8_f32 v27, v132, v133
	v_cvt_pk_fp8_f32 v26, v130, v131 op_sel:[0,0,1]
	v_mul_f32_e32 v136, v136, v9
	v_mul_f32_e32 v137, v137, v9
	v_mul_f32_e32 v138, v138, v9
	v_mul_f32_e32 v139, v139, v9
	v_mov_b32_e32 v28, v10
	v_cvt_pk_fp8_f32 v28, v136, v137
	v_cvt_pk_fp8_f32 v27, v134, v135 op_sel:[0,0,1]
	v_mul_f32_e32 v140, v140, v9
	v_mul_f32_e32 v141, v141, v9
	v_mul_f32_e32 v142, v142, v9
	v_mul_f32_e32 v143, v143, v9
	v_mov_b32_e32 v29, v10
	v_cvt_pk_fp8_f32 v29, v140, v141
	v_cvt_pk_fp8_f32 v28, v138, v139 op_sel:[0,0,1]
	v_mul_f32_e32 v144, v144, v9
	v_mul_f32_e32 v145, v145, v9
	v_mul_f32_e32 v146, v146, v9
	v_mul_f32_e32 v147, v147, v9
	v_mov_b32_e32 v30, v10
	v_cvt_pk_fp8_f32 v30, v144, v145
	v_cvt_pk_fp8_f32 v29, v142, v143 op_sel:[0,0,1]
	v_mul_f32_e32 v148, v148, v9
	v_mul_f32_e32 v149, v149, v9
	v_mul_f32_e32 v150, v150, v9
	v_mul_f32_e32 v151, v151, v9
	v_mov_b32_e32 v31, v10
	v_cvt_pk_fp8_f32 v31, v148, v149
	v_cvt_pk_fp8_f32 v30, v146, v147 op_sel:[0,0,1]
	v_mul_f32_e32 v152, v152, v9
	v_mul_f32_e32 v153, v153, v9
	v_mul_f32_e32 v154, v154, v9
	v_mul_f32_e32 v155, v155, v9
	v_mov_b32_e32 v32, v10
	v_cvt_pk_fp8_f32 v32, v152, v153
	v_cvt_pk_fp8_f32 v31, v150, v151 op_sel:[0,0,1]
	v_mul_f32_e32 v156, v156, v9
	v_mul_f32_e32 v157, v157, v9
	v_mul_f32_e32 v158, v158, v9
	v_mul_f32_e32 v159, v159, v9
	v_mov_b32_e32 v33, v10
	v_cvt_pk_fp8_f32 v33, v156, v157
	v_cvt_pk_fp8_f32 v32, v154, v155 op_sel:[0,0,1]
	v_mul_f32_e32 v160, v160, v9
	v_mul_f32_e32 v161, v161, v9
	v_mul_f32_e32 v162, v162, v9
	v_mul_f32_e32 v163, v163, v9
	v_mov_b32_e32 v34, v10
	v_cvt_pk_fp8_f32 v34, v160, v161
	v_cvt_pk_fp8_f32 v33, v158, v159 op_sel:[0,0,1]
	v_mul_f32_e32 v164, v164, v9
	v_mul_f32_e32 v165, v165, v9
	v_mul_f32_e32 v166, v166, v9
	v_mul_f32_e32 v167, v167, v9
	v_mov_b32_e32 v35, v10
	v_cvt_pk_fp8_f32 v35, v164, v165
	v_cvt_pk_fp8_f32 v34, v162, v163 op_sel:[0,0,1]
	v_cvt_pk_fp8_f32 v35, v166, v167 op_sel:[0,0,1]
	s_nop 0
	v_mul_f32_e32 v8, 0x3b800000, v6
	global_store_dword v2, v20, s[8:9]
	global_store_dword v2, v21, s[8:9] offset:256
	global_store_dword v2, v22, s[8:9] offset:512
	global_store_dword v2, v23, s[8:9] offset:768
	global_store_dword v2, v24, s[8:9] offset:1024
	global_store_dword v2, v25, s[8:9] offset:1280
	global_store_dword v2, v26, s[8:9] offset:1536
	global_store_dword v2, v27, s[8:9] offset:1792
; __device__ __forceinline__ void peer_row_load(f32x4 (&v)[16], const float* const (&in)[34], int it, int layer, int lane) {
;     const int tbl = it >= NEXP, r = it - tbl * NEXP + layer * NEXP;
;     const f32x4* src = (const f32x4*)((tbl ? in[33] : in[32]) + (size_t)r * D) + lane;
; #pragma unroll
;     for (int j = 0; j < 16; ++j) v[j] = src[64 * j];
; }
; __device__ __forceinline__ void peer_row_store(const f32x4 (&v)[16], unsigned char* ws, int it, int layer, int lane) {
;     const int tbl = it >= NEXP, r = it - tbl * NEXP + layer * NEXP;
;     float am = 0.f;
; #pragma unroll
;     for (int j = 0; j < 16; ++j) am = fmaxf(fmaxf(am, fmaxf(fabsf(v[j][0]), fabsf(v[j][1]))), fmaxf(fabsf(v[j][2]), fabsf(v[j][3])));
;     am = __uint_as_float(max64u(__float_as_uint(am)));
;     const float q = am > 0.f ? 256.0f / am : 0.f;
;     unsigned* dst = (unsigned*)(ws + (tbl ? WS_PV : WS_PU) + (size_t)r * D) + lane;
;     if (tbl) {
;         const int rl = it - NEXP;
;         unsigned char* pvl = ws + WS_PV + (size_t)layer * NEXP * D + (size_t)rl * 8 + (lane & 1) * 4;
;         unsigned char* pvg = ws + WS_PV + (size_t)layer * NEXP * D + (size_t)NEXP * 2048 + (size_t)rl * 2048 + 4 * lane;
; #pragma unroll
;         for (int j = 0; j < 16; ++j) { int w = __builtin_amdgcn_cvt_pk_bf8_f32(v[j][0] * q, v[j][1] * q, 0, false); w = __builtin_amdgcn_cvt_pk_bf8_f32(v[j][2] * q, v[j][3] * q, w, true);
;             if (j < 8) *(unsigned*)(pvl + (size_t)((lane >> 1) + 32 * j) * (NEXP * 8)) = (unsigned)w;
;             else *(unsigned*)(pvg + 256 * (j - 8)) = (unsigned)w; }
;     } else {
; #pragma unroll
;         for (int j = 0; j < 16; ++j) { int w = __builtin_amdgcn_cvt_pk_fp8_f32(v[j][0] * q, v[j][1] * q, 0, false); w = __builtin_amdgcn_cvt_pk_fp8_f32(v[j][2] * q, v[j][3] * q, w, true); dst[64 * j] = (unsigned)w; }
;     }
;     if (lane == 0) ((float*)(ws + (tbl ? WS_SV : WS_SU)))[r] = am * (1.0f / 256.0f);
	global_store_dword v2, v28, s[8:9] offset:2048
	global_store_dword v2, v29, s[8:9] offset:2304
	global_store_dword v2, v30, s[8:9] offset:2560
	global_store_dword v2, v31, s[8:9] offset:2816
	global_store_dword v2, v32, s[8:9] offset:3072
	global_store_dword v2, v33, s[8:9] offset:3328
	global_store_dword v2, v34, s[8:9] offset:3584
	global_store_dword v2, v35, s[8:9] offset:3840
	s_mov_b64 s[18:19], exec
	s_mov_b64 exec, s[12:13]
	global_store_dword v10, v8, s[10:11]
	s_mov_b64 exec, s[18:19]
	s_mov_b32 s4, s5
	s_add_i32 s5, s4, 1024
	s_lshl_b32 s1, s5, 14
	s_add_u32 s6, s84, s1
	s_addc_u32 s7, s85, 0
	global_load_dwordx4 v[104:107], v1, s[6:7]
	global_load_dwordx4 v[108:111], v1, s[6:7] offset:1024
	global_load_dwordx4 v[112:115], v1, s[6:7] offset:2048
	global_load_dwordx4 v[116:119], v1, s[6:7] offset:3072
	global_load_dwordx4 v[120:123], v3, s[6:7]
	global_load_dwordx4 v[124:127], v3, s[6:7] offset:1024
	global_load_dwordx4 v[128:131], v3, s[6:7] offset:2048
	global_load_dwordx4 v[132:135], v3, s[6:7] offset:3072
	global_load_dwordx4 v[136:139], v4, s[6:7]
	global_load_dwordx4 v[140:143], v4, s[6:7] offset:1024
	global_load_dwordx4 v[144:147], v4, s[6:7] offset:2048
	global_load_dwordx4 v[148:151], v4, s[6:7] offset:3072
	global_load_dwordx4 v[152:155], v5, s[6:7]
	global_load_dwordx4 v[156:159], v5, s[6:7] offset:1024
	global_load_dwordx4 v[160:163], v5, s[6:7] offset:2048
	global_load_dwordx4 v[164:167], v5, s[6:7] offset:3072
	s_waitcnt vmcnt(48)
	v_max3_f32 v6, |v40|, |v41|, 0
	v_max3_f32 v6, |v42|, |v43|, v6
	s_waitcnt vmcnt(47)
	v_max3_f32 v6, |v44|, |v45|, v6
	v_max3_f32 v6, |v46|, |v47|, v6
	s_waitcnt vmcnt(46)
	v_max3_f32 v6, |v48|, |v49|, v6
	v_max3_f32 v6, |v50|, |v51|, v6
	s_waitcnt vmcnt(45)
	v_max3_f32 v6, |v52|, |v53|, v6
	v_max3_f32 v6, |v54|, |v55|, v6
	s_waitcnt vmcnt(44)
	v_max3_f32 v6, |v56|, |v57|, v6
	v_max3_f32 v6, |v58|, |v59|, v6
	s_waitcnt vmcnt(43)
	v_max3_f32 v6, |v60|, |v61|, v6
	v_max3_f32 v6, |v62|, |v63|, v6
	s_waitcnt vmcnt(42)
	v_max3_f32 v6, |v64|, |v65|, v6
	v_max3_f32 v6, |v66|, |v67|, v6
	s_waitcnt vmcnt(41)
	v_max3_f32 v6, |v68|, |v69|, v6
	v_max3_f32 v6, |v70|, |v71|, v6
	s_waitcnt vmcnt(40)
	v_max3_f32 v6, |v72|, |v73|, v6
	v_max3_f32 v6, |v74|, |v75|, v6
	s_waitcnt vmcnt(39)
	v_max3_f32 v6, |v76|, |v77|, v6
	v_max3_f32 v6, |v78|, |v79|, v6
	s_waitcnt vmcnt(38)
	v_max3_f32 v6, |v80|, |v81|, v6
	v_max3_f32 v6, |v82|, |v83|, v6
	s_waitcnt vmcnt(37)
	v_max3_f32 v6, |v84|, |v85|, v6
	v_max3_f32 v6, |v86|, |v87|, v6
	s_waitcnt vmcnt(36)
	v_max3_f32 v6, |v88|, |v89|, v6
	v_max3_f32 v6, |v90|, |v91|, v6
	s_waitcnt vmcnt(35)
	v_max3_f32 v6, |v92|, |v93|, v6
	v_max3_f32 v6, |v94|, |v95|, v6
	s_waitcnt vmcnt(34)
	v_max3_f32 v6, |v96|, |v97|, v6
	v_max3_f32 v6, |v98|, |v99|, v6
	s_waitcnt vmcnt(33)
	v_max3_f32 v6, |v100|, |v101|, v6
	v_max3_f32 v6, |v102|, |v103|, v6
	s_nop 1
	v_max_u32_dpp v6, v6, v6 quad_perm:[1,0,3,2] row_mask:0xf bank_mask:0xf bound_ctrl:1
	s_nop 1
	v_max_u32_dpp v6, v6, v6 quad_perm:[2,3,0,1] row_mask:0xf bank_mask:0xf bound_ctrl:1
	s_nop 1
	v_max_u32_dpp v6, v6, v6 row_half_mirror row_mask:0xf bank_mask:0xf bound_ctrl:1
	s_nop 1
	v_max_u32_dpp v6, v6, v6 row_mirror row_mask:0xf bank_mask:0xf bound_ctrl:1
	s_nop 1
	v_mov_b32_e32 v7, v6
	s_nop 1
	v_permlane16_swap_b32_e32 v6, v7
	v_max_u32_e32 v6, v6, v7
	v_mov_b32_e32 v7, v6
	s_nop 1
	v_permlane32_swap_b32_e32 v6, v7
	v_max_u32_e32 v6, v6, v7
	v_div_scale_f32 v12, s[16:17], v6, v6, s14
	v_rcp_f32_e32 v13, v12
	s_nop 0
	v_fma_f32 v14, -v12, v13, 1.0
	v_fmac_f32_e32 v13, v14, v13
	v_div_scale_f32 v14, vcc, s14, v6, s14
	v_mul_f32_e32 v15, v14, v13
	v_fma_f32 v16, -v12, v15, v14
	v_fmac_f32_e32 v15, v16, v13
	v_fma_f32 v12, -v12, v15, v14
	v_div_fmas_f32 v12, v12, v13, v15
	v_div_fixup_f32 v9, v12, v6, s14
	v_cmp_lt_f32_e32 vcc, 0, v6
	s_nop 1
	v_cndmask_b32_e32 v9, 0, v9, vcc
	s_lshl_b32 s1, s4, 12
	s_add_u32 s8, s90, 0xba00000
	s_addc_u32 s9, s91, 0
	s_add_u32 s8, s8, s1
	s_addc_u32 s9, s9, 0
	s_lshl_b32 s1, s4, 2
	s_add_u32 s10, s90, 0x1ba00000
	s_addc_u32 s11, s91, 0
	s_add_u32 s10, s10, s1
	s_addc_u32 s11, s11, 0
	v_mul_f32_e32 v40, v40, v9
	v_mul_f32_e32 v41, v41, v9
	v_mul_f32_e32 v42, v42, v9
	v_mul_f32_e32 v43, v43, v9
	v_mov_b32_e32 v20, v10
	v_cvt_pk_fp8_f32 v20, v40, v41
	v_mul_f32_e32 v44, v44, v9
	v_mul_f32_e32 v45, v45, v9
	v_mul_f32_e32 v46, v46, v9
	v_mul_f32_e32 v47, v47, v9
	v_mov_b32_e32 v21, v10
	v_cvt_pk_fp8_f32 v21, v44, v45
	v_cvt_pk_fp8_f32 v20, v42, v43 op_sel:[0,0,1]
	v_mul_f32_e32 v48, v48, v9
	v_mul_f32_e32 v49, v49, v9
	v_mul_f32_e32 v50, v50, v9
	v_mul_f32_e32 v51, v51, v9
	v_mov_b32_e32 v22, v10
	v_cvt_pk_fp8_f32 v22, v48, v49
	v_cvt_pk_fp8_f32 v21, v46, v47 op_sel:[0,0,1]
	v_mul_f32_e32 v52, v52, v9
	v_mul_f32_e32 v53, v53, v9
	v_mul_f32_e32 v54, v54, v9
	v_mul_f32_e32 v55, v55, v9
	v_mov_b32_e32 v23, v10
	v_cvt_pk_fp8_f32 v23, v52, v53
	v_cvt_pk_fp8_f32 v22, v50, v51 op_sel:[0,0,1]
	v_mul_f32_e32 v56, v56, v9
	v_mul_f32_e32 v57, v57, v9
	v_mul_f32_e32 v58, v58, v9
	v_mul_f32_e32 v59, v59, v9
	v_mov_b32_e32 v24, v10
	v_cvt_pk_fp8_f32 v24, v56, v57
	v_cvt_pk_fp8_f32 v23, v54, v55 op_sel:[0,0,1]
	v_mul_f32_e32 v60, v60, v9
	v_mul_f32_e32 v61, v61, v9
	v_mul_f32_e32 v62, v62, v9
	v_mul_f32_e32 v63, v63, v9
	v_mov_b32_e32 v25, v10
	v_cvt_pk_fp8_f32 v25, v60, v61
	v_cvt_pk_fp8_f32 v24, v58, v59 op_sel:[0,0,1]
	v_mul_f32_e32 v64, v64, v9
	v_mul_f32_e32 v65, v65, v9
	v_mul_f32_e32 v66, v66, v9
	v_mul_f32_e32 v67, v67, v9
	v_mov_b32_e32 v26, v10
	v_cvt_pk_fp8_f32 v26, v64, v65
	v_cvt_pk_fp8_f32 v25, v62, v63 op_sel:[0,0,1]
	v_mul_f32_e32 v68, v68, v9
	v_mul_f32_e32 v69, v69, v9
	v_mul_f32_e32 v70, v70, v9
; __device__ __forceinline__ void peer_row_load(f32x4 (&v)[16], const float* const (&in)[34], int it, int layer, int lane) {
;     const int tbl = it >= NEXP, r = it - tbl * NEXP + layer * NEXP;
;     const f32x4* src = (const f32x4*)((tbl ? in[33] : in[32]) + (size_t)r * D) + lane;
; #pragma unroll
;     for (int j = 0; j < 16; ++j) v[j] = src[64 * j];
; }
; __device__ __forceinline__ void peer_row_store(const f32x4 (&v)[16], unsigned char* ws, int it, int layer, int lane) {
;     const int tbl = it >= NEXP, r = it - tbl * NEXP + layer * NEXP;
;     float am = 0.f;
; #pragma unroll
;     for (int j = 0; j < 16; ++j) am = fmaxf(fmaxf(am, fmaxf(fabsf(v[j][0]), fabsf(v[j][1]))), fmaxf(fabsf(v[j][2]), fabsf(v[j][3])));
;     am = __uint_as_float(max64u(__float_as_uint(am)));
;     const float q = am > 0.f ? 256.0f / am : 0.f;
;     unsigned* dst = (unsigned*)(ws + (tbl ? WS_PV : WS_PU) + (size_t)r * D) + lane;
;     if (tbl) {
;         const int rl = it - NEXP;
;         unsigned char* pvl = ws + WS_PV + (size_t)layer * NEXP * D + (size_t)rl * 8 + (lane & 1) * 4;
;         unsigned char* pvg = ws + WS_PV + (size_t)layer * NEXP * D + (size_t)NEXP * 2048 + (size_t)rl * 2048 + 4 * lane;
; #pragma unroll
;         for (int j = 0; j < 16; ++j) { int w = __builtin_amdgcn_cvt_pk_bf8_f32(v[j][0] * q, v[j][1] * q, 0, false); w = __builtin_amdgcn_cvt_pk_bf8_f32(v[j][2] * q, v[j][3] * q, w, true);
;             if (j < 8) *(unsigned*)(pvl + (size_t)((lane >> 1) + 32 * j) * (NEXP * 8)) = (unsigned)w;
;             else *(unsigned*)(pvg + 256 * (j - 8)) = (unsigned)w; }
;     } else {
; #pragma unroll
;         for (int j = 0; j < 16; ++j) { int w = __builtin_amdgcn_cvt_pk_fp8_f32(v[j][0] * q, v[j][1] * q, 0, false); w = __builtin_amdgcn_cvt_pk_fp8_f32(v[j][2] * q, v[j][3] * q, w, true); dst[64 * j] = (unsigned)w; }
;     }
;     if (lane == 0) ((float*)(ws + (tbl ? WS_SV : WS_SU)))[r] = am * (1.0f / 256.0f);
	v_mul_f32_e32 v71, v71, v9
	v_mov_b32_e32 v27, v10
	v_cvt_pk_fp8_f32 v27, v68, v69
	v_cvt_pk_fp8_f32 v26, v66, v67 op_sel:[0,0,1]
	v_mul_f32_e32 v72, v72, v9
	v_mul_f32_e32 v73, v73, v9
	v_mul_f32_e32 v74, v74, v9
	v_mul_f32_e32 v75, v75, v9
	v_mov_b32_e32 v28, v10
	v_cvt_pk_fp8_f32 v28, v72, v73
	v_cvt_pk_fp8_f32 v27, v70, v71 op_sel:[0,0,1]
	v_mul_f32_e32 v76, v76, v9
	v_mul_f32_e32 v77, v77, v9
	v_mul_f32_e32 v78, v78, v9
	v_mul_f32_e32 v79, v79, v9
	v_mov_b32_e32 v29, v10
	v_cvt_pk_fp8_f32 v29, v76, v77
	v_cvt_pk_fp8_f32 v28, v74, v75 op_sel:[0,0,1]
	v_mul_f32_e32 v80, v80, v9
	v_mul_f32_e32 v81, v81, v9
	v_mul_f32_e32 v82, v82, v9
	v_mul_f32_e32 v83, v83, v9
	v_mov_b32_e32 v30, v10
	v_cvt_pk_fp8_f32 v30, v80, v81
	v_cvt_pk_fp8_f32 v29, v78, v79 op_sel:[0,0,1]
	v_mul_f32_e32 v84, v84, v9
	v_mul_f32_e32 v85, v85, v9
	v_mul_f32_e32 v86, v86, v9
	v_mul_f32_e32 v87, v87, v9
	v_mov_b32_e32 v31, v10
	v_cvt_pk_fp8_f32 v31, v84, v85
	v_cvt_pk_fp8_f32 v30, v82, v83 op_sel:[0,0,1]
	v_mul_f32_e32 v88, v88, v9
	v_mul_f32_e32 v89, v89, v9
	v_mul_f32_e32 v90, v90, v9
	v_mul_f32_e32 v91, v91, v9
	v_mov_b32_e32 v32, v10
	v_cvt_pk_fp8_f32 v32, v88, v89
	v_cvt_pk_fp8_f32 v31, v86, v87 op_sel:[0,0,1]
	v_mul_f32_e32 v92, v92, v9
	v_mul_f32_e32 v93, v93, v9
	v_mul_f32_e32 v94, v94, v9
	v_mul_f32_e32 v95, v95, v9
	v_mov_b32_e32 v33, v10
	v_cvt_pk_fp8_f32 v33, v92, v93
	v_cvt_pk_fp8_f32 v32, v90, v91 op_sel:[0,0,1]
	v_mul_f32_e32 v96, v96, v9
	v_mul_f32_e32 v97, v97, v9
	v_mul_f32_e32 v98, v98, v9
	v_mul_f32_e32 v99, v99, v9
	v_mov_b32_e32 v34, v10
	v_cvt_pk_fp8_f32 v34, v96, v97
	v_cvt_pk_fp8_f32 v33, v94, v95 op_sel:[0,0,1]
	v_mul_f32_e32 v100, v100, v9
	v_mul_f32_e32 v101, v101, v9
	v_mul_f32_e32 v102, v102, v9
	v_mul_f32_e32 v103, v103, v9
	v_mov_b32_e32 v35, v10
	v_cvt_pk_fp8_f32 v35, v100, v101
	v_cvt_pk_fp8_f32 v34, v98, v99 op_sel:[0,0,1]
	v_cvt_pk_fp8_f32 v35, v102, v103 op_sel:[0,0,1]
	s_nop 0
	v_mul_f32_e32 v8, 0x3b800000, v6
	global_store_dword v2, v20, s[8:9]
	global_store_dword v2, v21, s[8:9] offset:256
	global_store_dword v2, v22, s[8:9] offset:512
	global_store_dword v2, v23, s[8:9] offset:768
	global_store_dword v2, v24, s[8:9] offset:1024
	global_store_dword v2, v25, s[8:9] offset:1280
	global_store_dword v2, v26, s[8:9] offset:1536
	global_store_dword v2, v27, s[8:9] offset:1792
	global_store_dword v2, v28, s[8:9] offset:2048
	global_store_dword v2, v29, s[8:9] offset:2304
	global_store_dword v2, v30, s[8:9] offset:2560
	global_store_dword v2, v31, s[8:9] offset:2816
	global_store_dword v2, v32, s[8:9] offset:3072
	global_store_dword v2, v33, s[8:9] offset:3328
	global_store_dword v2, v34, s[8:9] offset:3584
	global_store_dword v2, v35, s[8:9] offset:3840
	s_mov_b64 s[18:19], exec
	s_mov_b64 exec, s[12:13]
	global_store_dword v10, v8, s[10:11]
	s_mov_b64 exec, s[18:19]
	s_mov_b32 s4, s5
	s_add_i32 s5, s4, 1024
	s_lshl_b32 s1, s5, 14
	s_add_u32 s6, s84, s1
	s_addc_u32 s7, s85, 0
	global_load_dwordx4 v[40:43], v1, s[6:7]
	global_load_dwordx4 v[44:47], v1, s[6:7] offset:1024
	global_load_dwordx4 v[48:51], v1, s[6:7] offset:2048
	global_load_dwordx4 v[52:55], v1, s[6:7] offset:3072
	global_load_dwordx4 v[56:59], v3, s[6:7]
	global_load_dwordx4 v[60:63], v3, s[6:7] offset:1024
	global_load_dwordx4 v[64:67], v3, s[6:7] offset:2048
	global_load_dwordx4 v[68:71], v3, s[6:7] offset:3072
	global_load_dwordx4 v[72:75], v4, s[6:7]
	global_load_dwordx4 v[76:79], v4, s[6:7] offset:1024
	global_load_dwordx4 v[80:83], v4, s[6:7] offset:2048
	global_load_dwordx4 v[84:87], v4, s[6:7] offset:3072
	global_load_dwordx4 v[88:91], v5, s[6:7]
	global_load_dwordx4 v[92:95], v5, s[6:7] offset:1024
	global_load_dwordx4 v[96:99], v5, s[6:7] offset:2048
	global_load_dwordx4 v[100:103], v5, s[6:7] offset:3072
	s_waitcnt vmcnt(48)
	v_max3_f32 v6, |v104|, |v105|, 0
	v_max3_f32 v6, |v106|, |v107|, v6
	s_waitcnt vmcnt(47)
	v_max3_f32 v6, |v108|, |v109|, v6
	v_max3_f32 v6, |v110|, |v111|, v6
	s_waitcnt vmcnt(46)
	v_max3_f32 v6, |v112|, |v113|, v6
	v_max3_f32 v6, |v114|, |v115|, v6
	s_waitcnt vmcnt(45)
	v_max3_f32 v6, |v116|, |v117|, v6
	v_max3_f32 v6, |v118|, |v119|, v6
	s_waitcnt vmcnt(44)
	v_max3_f32 v6, |v120|, |v121|, v6
	v_max3_f32 v6, |v122|, |v123|, v6
	s_waitcnt vmcnt(43)
	v_max3_f32 v6, |v124|, |v125|, v6
	v_max3_f32 v6, |v126|, |v127|, v6
	s_waitcnt vmcnt(42)
	v_max3_f32 v6, |v128|, |v129|, v6
	v_max3_f32 v6, |v130|, |v131|, v6
	s_waitcnt vmcnt(41)
	v_max3_f32 v6, |v132|, |v133|, v6
	v_max3_f32 v6, |v134|, |v135|, v6
	s_waitcnt vmcnt(40)
	v_max3_f32 v6, |v136|, |v137|, v6
	v_max3_f32 v6, |v138|, |v139|, v6
	s_waitcnt vmcnt(39)
	v_max3_f32 v6, |v140|, |v141|, v6
	v_max3_f32 v6, |v142|, |v143|, v6
	s_waitcnt vmcnt(38)
	v_max3_f32 v6, |v144|, |v145|, v6
	v_max3_f32 v6, |v146|, |v147|, v6
	s_waitcnt vmcnt(37)
	v_max3_f32 v6, |v148|, |v149|, v6
	v_max3_f32 v6, |v150|, |v151|, v6
	s_waitcnt vmcnt(36)
	v_max3_f32 v6, |v152|, |v153|, v6
	v_max3_f32 v6, |v154|, |v155|, v6
	s_waitcnt vmcnt(35)
	v_max3_f32 v6, |v156|, |v157|, v6
	v_max3_f32 v6, |v158|, |v159|, v6
	s_waitcnt vmcnt(34)
	v_max3_f32 v6, |v160|, |v161|, v6
	v_max3_f32 v6, |v162|, |v163|, v6
	s_waitcnt vmcnt(33)
; __device__ __forceinline__ void peer_row_load(f32x4 (&v)[16], const float* const (&in)[34], int it, int layer, int lane) {
;     const int tbl = it >= NEXP, r = it - tbl * NEXP + layer * NEXP;
;     const f32x4* src = (const f32x4*)((tbl ? in[33] : in[32]) + (size_t)r * D) + lane;
; #pragma unroll
;     for (int j = 0; j < 16; ++j) v[j] = src[64 * j];
; }
; __device__ __forceinline__ void peer_row_store(const f32x4 (&v)[16], unsigned char* ws, int it, int layer, int lane) {
;     const int tbl = it >= NEXP, r = it - tbl * NEXP + layer * NEXP;
;     float am = 0.f;
; #pragma unroll
;     for (int j = 0; j < 16; ++j) am = fmaxf(fmaxf(am, fmaxf(fabsf(v[j][0]), fabsf(v[j][1]))), fmaxf(fabsf(v[j][2]), fabsf(v[j][3])));
;     am = __uint_as_float(max64u(__float_as_uint(am)));
;     const float q = am > 0.f ? 256.0f / am : 0.f;
;     unsigned* dst = (unsigned*)(ws + (tbl ? WS_PV : WS_PU) + (size_t)r * D) + lane;
;     if (tbl) {
;         const int rl = it - NEXP;
;         unsigned char* pvl = ws + WS_PV + (size_t)layer * NEXP * D + (size_t)rl * 8 + (lane & 1) * 4;
;         unsigned char* pvg = ws + WS_PV + (size_t)layer * NEXP * D + (size_t)NEXP * 2048 + (size_t)rl * 2048 + 4 * lane;
; #pragma unroll
;         for (int j = 0; j < 16; ++j) { int w = __builtin_amdgcn_cvt_pk_bf8_f32(v[j][0] * q, v[j][1] * q, 0, false); w = __builtin_amdgcn_cvt_pk_bf8_f32(v[j][2] * q, v[j][3] * q, w, true);
;             if (j < 8) *(unsigned*)(pvl + (size_t)((lane >> 1) + 32 * j) * (NEXP * 8)) = (unsigned)w;
;             else *(unsigned*)(pvg + 256 * (j - 8)) = (unsigned)w; }
;     } else {
; #pragma unroll
;         for (int j = 0; j < 16; ++j) { int w = __builtin_amdgcn_cvt_pk_fp8_f32(v[j][0] * q, v[j][1] * q, 0, false); w = __builtin_amdgcn_cvt_pk_fp8_f32(v[j][2] * q, v[j][3] * q, w, true); dst[64 * j] = (unsigned)w; }
;     }
;     if (lane == 0) ((float*)(ws + (tbl ? WS_SV : WS_SU)))[r] = am * (1.0f / 256.0f);
	v_max3_f32 v6, |v164|, |v165|, v6
	v_max3_f32 v6, |v166|, |v167|, v6
	s_nop 1
	v_max_u32_dpp v6, v6, v6 quad_perm:[1,0,3,2] row_mask:0xf bank_mask:0xf bound_ctrl:1
	s_nop 1
	v_max_u32_dpp v6, v6, v6 quad_perm:[2,3,0,1] row_mask:0xf bank_mask:0xf bound_ctrl:1
	s_nop 1
	v_max_u32_dpp v6, v6, v6 row_half_mirror row_mask:0xf bank_mask:0xf bound_ctrl:1
	s_nop 1
	v_max_u32_dpp v6, v6, v6 row_mirror row_mask:0xf bank_mask:0xf bound_ctrl:1
	s_nop 1
	v_mov_b32_e32 v7, v6
	s_nop 1
	v_permlane16_swap_b32_e32 v6, v7
	v_max_u32_e32 v6, v6, v7
	v_mov_b32_e32 v7, v6
	s_nop 1
	v_permlane32_swap_b32_e32 v6, v7
	v_max_u32_e32 v6, v6, v7
	v_div_scale_f32 v12, s[16:17], v6, v6, s14
	v_rcp_f32_e32 v13, v12
	s_nop 0
	v_fma_f32 v14, -v12, v13, 1.0
	v_fmac_f32_e32 v13, v14, v13
	v_div_scale_f32 v14, vcc, s14, v6, s14
	v_mul_f32_e32 v15, v14, v13
	v_fma_f32 v16, -v12, v15, v14
	v_fmac_f32_e32 v15, v16, v13
	v_fma_f32 v12, -v12, v15, v14
	v_div_fmas_f32 v12, v12, v13, v15
	v_div_fixup_f32 v9, v12, v6, s14
	v_cmp_lt_f32_e32 vcc, 0, v6
	s_nop 1
	v_cndmask_b32_e32 v9, 0, v9, vcc
	s_lshl_b32 s1, s4, 12
	s_add_u32 s8, s90, 0xba00000
	s_addc_u32 s9, s91, 0
	s_add_u32 s8, s8, s1
	s_addc_u32 s9, s9, 0
	s_lshl_b32 s1, s4, 2
	s_add_u32 s10, s90, 0x1ba00000
	s_addc_u32 s11, s91, 0
	s_add_u32 s10, s10, s1
	s_addc_u32 s11, s11, 0
	v_mul_f32_e32 v104, v104, v9
	v_mul_f32_e32 v105, v105, v9
	v_mul_f32_e32 v106, v106, v9
	v_mul_f32_e32 v107, v107, v9
	v_mov_b32_e32 v20, v10
	v_cvt_pk_fp8_f32 v20, v104, v105
	v_mul_f32_e32 v108, v108, v9
	v_mul_f32_e32 v109, v109, v9
	v_mul_f32_e32 v110, v110, v9
	v_mul_f32_e32 v111, v111, v9
	v_mov_b32_e32 v21, v10
	v_cvt_pk_fp8_f32 v21, v108, v109
	v_cvt_pk_fp8_f32 v20, v106, v107 op_sel:[0,0,1]
	v_mul_f32_e32 v112, v112, v9
	v_mul_f32_e32 v113, v113, v9
	v_mul_f32_e32 v114, v114, v9
	v_mul_f32_e32 v115, v115, v9
	v_mov_b32_e32 v22, v10
	v_cvt_pk_fp8_f32 v22, v112, v113
	v_cvt_pk_fp8_f32 v21, v110, v111 op_sel:[0,0,1]
	v_mul_f32_e32 v116, v116, v9
	v_mul_f32_e32 v117, v117, v9
	v_mul_f32_e32 v118, v118, v9
	v_mul_f32_e32 v119, v119, v9
	v_mov_b32_e32 v23, v10
	v_cvt_pk_fp8_f32 v23, v116, v117
	v_cvt_pk_fp8_f32 v22, v114, v115 op_sel:[0,0,1]
	v_mul_f32_e32 v120, v120, v9
	v_mul_f32_e32 v121, v121, v9
	v_mul_f32_e32 v122, v122, v9
	v_mul_f32_e32 v123, v123, v9
	v_mov_b32_e32 v24, v10
	v_cvt_pk_fp8_f32 v24, v120, v121
	v_cvt_pk_fp8_f32 v23, v118, v119 op_sel:[0,0,1]
	v_mul_f32_e32 v124, v124, v9
	v_mul_f32_e32 v125, v125, v9
	v_mul_f32_e32 v126, v126, v9
	v_mul_f32_e32 v127, v127, v9
	v_mov_b32_e32 v25, v10
	v_cvt_pk_fp8_f32 v25, v124, v125
	v_cvt_pk_fp8_f32 v24, v122, v123 op_sel:[0,0,1]
	v_mul_f32_e32 v128, v128, v9
	v_mul_f32_e32 v129, v129, v9
	v_mul_f32_e32 v130, v130, v9
	v_mul_f32_e32 v131, v131, v9
	v_mov_b32_e32 v26, v10
	v_cvt_pk_fp8_f32 v26, v128, v129
	v_cvt_pk_fp8_f32 v25, v126, v127 op_sel:[0,0,1]
	v_mul_f32_e32 v132, v132, v9
	v_mul_f32_e32 v133, v133, v9
	v_mul_f32_e32 v134, v134, v9
	v_mul_f32_e32 v135, v135, v9
	v_mov_b32_e32 v27, v10
	v_cvt_pk_fp8_f32 v27, v132, v133
	v_cvt_pk_fp8_f32 v26, v130, v131 op_sel:[0,0,1]
	v_mul_f32_e32 v136, v136, v9
	v_mul_f32_e32 v137, v137, v9
	v_mul_f32_e32 v138, v138, v9
	v_mul_f32_e32 v139, v139, v9
	v_mov_b32_e32 v28, v10
	v_cvt_pk_fp8_f32 v28, v136, v137
	v_cvt_pk_fp8_f32 v27, v134, v135 op_sel:[0,0,1]
	v_mul_f32_e32 v140, v140, v9
	v_mul_f32_e32 v141, v141, v9
	v_mul_f32_e32 v142, v142, v9
	v_mul_f32_e32 v143, v143, v9
	v_mov_b32_e32 v29, v10
	v_cvt_pk_fp8_f32 v29, v140, v141
	v_cvt_pk_fp8_f32 v28, v138, v139 op_sel:[0,0,1]
	v_mul_f32_e32 v144, v144, v9
	v_mul_f32_e32 v145, v145, v9
	v_mul_f32_e32 v146, v146, v9
	v_mul_f32_e32 v147, v147, v9
	v_mov_b32_e32 v30, v10
	v_cvt_pk_fp8_f32 v30, v144, v145
	v_cvt_pk_fp8_f32 v29, v142, v143 op_sel:[0,0,1]
	v_mul_f32_e32 v148, v148, v9
	v_mul_f32_e32 v149, v149, v9
	v_mul_f32_e32 v150, v150, v9
	v_mul_f32_e32 v151, v151, v9
	v_mov_b32_e32 v31, v10
	v_cvt_pk_fp8_f32 v31, v148, v149
	v_cvt_pk_fp8_f32 v30, v146, v147 op_sel:[0,0,1]
	v_mul_f32_e32 v152, v152, v9
	v_mul_f32_e32 v153, v153, v9
	v_mul_f32_e32 v154, v154, v9
	v_mul_f32_e32 v155, v155, v9
	v_mov_b32_e32 v32, v10
	v_cvt_pk_fp8_f32 v32, v152, v153
	v_cvt_pk_fp8_f32 v31, v150, v151 op_sel:[0,0,1]
	v_mul_f32_e32 v156, v156, v9
	v_mul_f32_e32 v157, v157, v9
	v_mul_f32_e32 v158, v158, v9
	v_mul_f32_e32 v159, v159, v9
	v_mov_b32_e32 v33, v10
	v_cvt_pk_fp8_f32 v33, v156, v157
	v_cvt_pk_fp8_f32 v32, v154, v155 op_sel:[0,0,1]
	v_mul_f32_e32 v160, v160, v9
	v_mul_f32_e32 v161, v161, v9
	v_mul_f32_e32 v162, v162, v9
	v_mul_f32_e32 v163, v163, v9
	v_mov_b32_e32 v34, v10
	v_cvt_pk_fp8_f32 v34, v160, v161
	v_cvt_pk_fp8_f32 v33, v158, v159 op_sel:[0,0,1]
	v_mul_f32_e32 v164, v164, v9
	v_mul_f32_e32 v165, v165, v9
	v_mul_f32_e32 v166, v166, v9
	v_mul_f32_e32 v167, v167, v9
	v_mov_b32_e32 v35, v10
	v_cvt_pk_fp8_f32 v35, v164, v165
	v_cvt_pk_fp8_f32 v34, v162, v163 op_sel:[0,0,1]
	v_cvt_pk_fp8_f32 v35, v166, v167 op_sel:[0,0,1]
	s_nop 0
	v_mul_f32_e32 v8, 0x3b800000, v6
	global_store_dword v2, v20, s[8:9]
	global_store_dword v2, v21, s[8:9] offset:256
	global_store_dword v2, v22, s[8:9] offset:512
	global_store_dword v2, v23, s[8:9] offset:768
	global_store_dword v2, v24, s[8:9] offset:1024
	global_store_dword v2, v25, s[8:9] offset:1280
	global_store_dword v2, v26, s[8:9] offset:1536
	global_store_dword v2, v27, s[8:9] offset:1792
	global_store_dword v2, v28, s[8:9] offset:2048
	global_store_dword v2, v29, s[8:9] offset:2304
	global_store_dword v2, v30, s[8:9] offset:2560
	global_store_dword v2, v31, s[8:9] offset:2816
	global_store_dword v2, v32, s[8:9] offset:3072
	global_store_dword v2, v33, s[8:9] offset:3328
	global_store_dword v2, v34, s[8:9] offset:3584
	global_store_dword v2, v35, s[8:9] offset:3840
	s_mov_b64 s[18:19], exec
	s_mov_b64 exec, s[12:13]
	global_store_dword v10, v8, s[10:11]
	s_mov_b64 exec, s[18:19]
	s_mov_b32 s4, s5
	s_add_i32 s5, s4, 1024
	s_lshl_b32 s1, s5, 14
	s_add_u32 s6, s84, s1
	s_addc_u32 s7, s85, 0
	global_load_dwordx4 v[104:107], v1, s[6:7]
	global_load_dwordx4 v[108:111], v1, s[6:7] offset:1024
	global_load_dwordx4 v[112:115], v1, s[6:7] offset:2048
	global_load_dwordx4 v[116:119], v1, s[6:7] offset:3072
	global_load_dwordx4 v[120:123], v3, s[6:7]
	global_load_dwordx4 v[124:127], v3, s[6:7] offset:1024
	global_load_dwordx4 v[128:131], v3, s[6:7] offset:2048
	global_load_dwordx4 v[132:135], v3, s[6:7] offset:3072
	global_load_dwordx4 v[136:139], v4, s[6:7]
	global_load_dwordx4 v[140:143], v4, s[6:7] offset:1024
	global_load_dwordx4 v[144:147], v4, s[6:7] offset:2048
	global_load_dwordx4 v[148:151], v4, s[6:7] offset:3072
	global_load_dwordx4 v[152:155], v5, s[6:7]
	global_load_dwordx4 v[156:159], v5, s[6:7] offset:1024
	global_load_dwordx4 v[160:163], v5, s[6:7] offset:2048
	global_load_dwordx4 v[164:167], v5, s[6:7] offset:3072
	s_waitcnt vmcnt(48)
; __device__ __forceinline__ void peer_row_load(f32x4 (&v)[16], const float* const (&in)[34], int it, int layer, int lane) {
;     const int tbl = it >= NEXP, r = it - tbl * NEXP + layer * NEXP;
;     const f32x4* src = (const f32x4*)((tbl ? in[33] : in[32]) + (size_t)r * D) + lane;
; #pragma unroll
;     for (int j = 0; j < 16; ++j) v[j] = src[64 * j];
; }
; __device__ __forceinline__ void peer_row_store(const f32x4 (&v)[16], unsigned char* ws, int it, int layer, int lane) {
;     const int tbl = it >= NEXP, r = it - tbl * NEXP + layer * NEXP;
;     float am = 0.f;
; #pragma unroll
;     for (int j = 0; j < 16; ++j) am = fmaxf(fmaxf(am, fmaxf(fabsf(v[j][0]), fabsf(v[j][1]))), fmaxf(fabsf(v[j][2]), fabsf(v[j][3])));
;     am = __uint_as_float(max64u(__float_as_uint(am)));
;     const float q = am > 0.f ? 256.0f / am : 0.f;
;     unsigned* dst = (unsigned*)(ws + (tbl ? WS_PV : WS_PU) + (size_t)r * D) + lane;
;     if (tbl) {
;         const int rl = it - NEXP;
;         unsigned char* pvl = ws + WS_PV + (size_t)layer * NEXP * D + (size_t)rl * 8 + (lane & 1) * 4;
;         unsigned char* pvg = ws + WS_PV + (size_t)layer * NEXP * D + (size_t)NEXP * 2048 + (size_t)rl * 2048 + 4 * lane;
; #pragma unroll
;         for (int j = 0; j < 16; ++j) { int w = __builtin_amdgcn_cvt_pk_bf8_f32(v[j][0] * q, v[j][1] * q, 0, false); w = __builtin_amdgcn_cvt_pk_bf8_f32(v[j][2] * q, v[j][3] * q, w, true);
;             if (j < 8) *(unsigned*)(pvl + (size_t)((lane >> 1) + 32 * j) * (NEXP * 8)) = (unsigned)w;
;             else *(unsigned*)(pvg + 256 * (j - 8)) = (unsigned)w; }
;     } else {
; #pragma unroll
;         for (int j = 0; j < 16; ++j) { int w = __builtin_amdgcn_cvt_pk_fp8_f32(v[j][0] * q, v[j][1] * q, 0, false); w = __builtin_amdgcn_cvt_pk_fp8_f32(v[j][2] * q, v[j][3] * q, w, true); dst[64 * j] = (unsigned)w; }
;     }
;     if (lane == 0) ((float*)(ws + (tbl ? WS_SV : WS_SU)))[r] = am * (1.0f / 256.0f);
	v_max3_f32 v6, |v40|, |v41|, 0
	v_max3_f32 v6, |v42|, |v43|, v6
	s_waitcnt vmcnt(47)
	v_max3_f32 v6, |v44|, |v45|, v6
	v_max3_f32 v6, |v46|, |v47|, v6
	s_waitcnt vmcnt(46)
	v_max3_f32 v6, |v48|, |v49|, v6
	v_max3_f32 v6, |v50|, |v51|, v6
	s_waitcnt vmcnt(45)
	v_max3_f32 v6, |v52|, |v53|, v6
	v_max3_f32 v6, |v54|, |v55|, v6
	s_waitcnt vmcnt(44)
	v_max3_f32 v6, |v56|, |v57|, v6
	v_max3_f32 v6, |v58|, |v59|, v6
	s_waitcnt vmcnt(43)
	v_max3_f32 v6, |v60|, |v61|, v6
	v_max3_f32 v6, |v62|, |v63|, v6
	s_waitcnt vmcnt(42)
	v_max3_f32 v6, |v64|, |v65|, v6
	v_max3_f32 v6, |v66|, |v67|, v6
	s_waitcnt vmcnt(41)
	v_max3_f32 v6, |v68|, |v69|, v6
	v_max3_f32 v6, |v70|, |v71|, v6
	s_waitcnt vmcnt(40)
	v_max3_f32 v6, |v72|, |v73|, v6
	v_max3_f32 v6, |v74|, |v75|, v6
	s_waitcnt vmcnt(39)
	v_max3_f32 v6, |v76|, |v77|, v6
	v_max3_f32 v6, |v78|, |v79|, v6
	s_waitcnt vmcnt(38)
	v_max3_f32 v6, |v80|, |v81|, v6
	v_max3_f32 v6, |v82|, |v83|, v6
	s_waitcnt vmcnt(37)
	v_max3_f32 v6, |v84|, |v85|, v6
	v_max3_f32 v6, |v86|, |v87|, v6
	s_waitcnt vmcnt(36)
	v_max3_f32 v6, |v88|, |v89|, v6
	v_max3_f32 v6, |v90|, |v91|, v6
	s_waitcnt vmcnt(35)
	v_max3_f32 v6, |v92|, |v93|, v6
	v_max3_f32 v6, |v94|, |v95|, v6
	s_waitcnt vmcnt(34)
	v_max3_f32 v6, |v96|, |v97|, v6
	v_max3_f32 v6, |v98|, |v99|, v6
	s_waitcnt vmcnt(33)
	v_max3_f32 v6, |v100|, |v101|, v6
	v_max3_f32 v6, |v102|, |v103|, v6
	s_nop 1
	v_max_u32_dpp v6, v6, v6 quad_perm:[1,0,3,2] row_mask:0xf bank_mask:0xf bound_ctrl:1
	s_nop 1
	v_max_u32_dpp v6, v6, v6 quad_perm:[2,3,0,1] row_mask:0xf bank_mask:0xf bound_ctrl:1
	s_nop 1
	v_max_u32_dpp v6, v6, v6 row_half_mirror row_mask:0xf bank_mask:0xf bound_ctrl:1
	s_nop 1
	v_max_u32_dpp v6, v6, v6 row_mirror row_mask:0xf bank_mask:0xf bound_ctrl:1
	s_nop 1
	v_mov_b32_e32 v7, v6
	s_nop 1
	v_permlane16_swap_b32_e32 v6, v7
	v_max_u32_e32 v6, v6, v7
	v_mov_b32_e32 v7, v6
	s_nop 1
	v_permlane32_swap_b32_e32 v6, v7
	v_max_u32_e32 v6, v6, v7
	v_div_scale_f32 v12, s[16:17], v6, v6, s14
	v_rcp_f32_e32 v13, v12
	s_nop 0
	v_fma_f32 v14, -v12, v13, 1.0
	v_fmac_f32_e32 v13, v14, v13
	v_div_scale_f32 v14, vcc, s14, v6, s14
	v_mul_f32_e32 v15, v14, v13
	v_fma_f32 v16, -v12, v15, v14
	v_fmac_f32_e32 v15, v16, v13
	v_fma_f32 v12, -v12, v15, v14
	v_div_fmas_f32 v12, v12, v13, v15
	v_div_fixup_f32 v9, v12, v6, s14
	v_cmp_lt_f32_e32 vcc, 0, v6
	s_nop 1
	v_cndmask_b32_e32 v9, 0, v9, vcc
	s_lshl_b32 s1, s4, 12
	s_add_u32 s8, s90, 0xba00000
	s_addc_u32 s9, s91, 0
	s_add_u32 s8, s8, s1
	s_addc_u32 s9, s9, 0
	s_lshl_b32 s1, s4, 2
	s_add_u32 s10, s90, 0x1ba00000
	s_addc_u32 s11, s91, 0
	s_add_u32 s10, s10, s1
	s_addc_u32 s11, s11, 0
	v_mul_f32_e32 v40, v40, v9
	v_mul_f32_e32 v41, v41, v9
	v_mul_f32_e32 v42, v42, v9
	v_mul_f32_e32 v43, v43, v9
	v_mov_b32_e32 v20, v10
	v_cvt_pk_fp8_f32 v20, v40, v41
	v_mul_f32_e32 v44, v44, v9
	v_mul_f32_e32 v45, v45, v9
	v_mul_f32_e32 v46, v46, v9
	v_mul_f32_e32 v47, v47, v9
	v_mov_b32_e32 v21, v10
	v_cvt_pk_fp8_f32 v21, v44, v45
	v_cvt_pk_fp8_f32 v20, v42, v43 op_sel:[0,0,1]
	v_mul_f32_e32 v48, v48, v9
	v_mul_f32_e32 v49, v49, v9
	v_mul_f32_e32 v50, v50, v9
	v_mul_f32_e32 v51, v51, v9
	v_mov_b32_e32 v22, v10
	v_cvt_pk_fp8_f32 v22, v48, v49
	v_cvt_pk_fp8_f32 v21, v46, v47 op_sel:[0,0,1]
	v_mul_f32_e32 v52, v52, v9
	v_mul_f32_e32 v53, v53, v9
	v_mul_f32_e32 v54, v54, v9
	v_mul_f32_e32 v55, v55, v9
	v_mov_b32_e32 v23, v10
	v_cvt_pk_fp8_f32 v23, v52, v53
	v_cvt_pk_fp8_f32 v22, v50, v51 op_sel:[0,0,1]
	v_mul_f32_e32 v56, v56, v9
	v_mul_f32_e32 v57, v57, v9
	v_mul_f32_e32 v58, v58, v9
	v_mul_f32_e32 v59, v59, v9
	v_mov_b32_e32 v24, v10
	v_cvt_pk_fp8_f32 v24, v56, v57
	v_cvt_pk_fp8_f32 v23, v54, v55 op_sel:[0,0,1]
	v_mul_f32_e32 v60, v60, v9
	v_mul_f32_e32 v61, v61, v9
	v_mul_f32_e32 v62, v62, v9
	v_mul_f32_e32 v63, v63, v9
	v_mov_b32_e32 v25, v10
	v_cvt_pk_fp8_f32 v25, v60, v61
	v_cvt_pk_fp8_f32 v24, v58, v59 op_sel:[0,0,1]
	v_mul_f32_e32 v64, v64, v9
	v_mul_f32_e32 v65, v65, v9
	v_mul_f32_e32 v66, v66, v9
	v_mul_f32_e32 v67, v67, v9
	v_mov_b32_e32 v26, v10
	v_cvt_pk_fp8_f32 v26, v64, v65
	v_cvt_pk_fp8_f32 v25, v62, v63 op_sel:[0,0,1]
	v_mul_f32_e32 v68, v68, v9
	v_mul_f32_e32 v69, v69, v9
	v_mul_f32_e32 v70, v70, v9
	v_mul_f32_e32 v71, v71, v9
	v_mov_b32_e32 v27, v10
	v_cvt_pk_fp8_f32 v27, v68, v69
	v_cvt_pk_fp8_f32 v26, v66, v67 op_sel:[0,0,1]
	v_mul_f32_e32 v72, v72, v9
	v_mul_f32_e32 v73, v73, v9
	v_mul_f32_e32 v74, v74, v9
	v_mul_f32_e32 v75, v75, v9
	v_mov_b32_e32 v28, v10
	v_cvt_pk_fp8_f32 v28, v72, v73
	v_cvt_pk_fp8_f32 v27, v70, v71 op_sel:[0,0,1]
	v_mul_f32_e32 v76, v76, v9
	v_mul_f32_e32 v77, v77, v9
	v_mul_f32_e32 v78, v78, v9
	v_mul_f32_e32 v79, v79, v9
	v_mov_b32_e32 v29, v10
	v_cvt_pk_fp8_f32 v29, v76, v77
	v_cvt_pk_fp8_f32 v28, v74, v75 op_sel:[0,0,1]
	v_mul_f32_e32 v80, v80, v9
	v_mul_f32_e32 v81, v81, v9
	v_mul_f32_e32 v82, v82, v9
	v_mul_f32_e32 v83, v83, v9
	v_mov_b32_e32 v30, v10
	v_cvt_pk_fp8_f32 v30, v80, v81
	v_cvt_pk_fp8_f32 v29, v78, v79 op_sel:[0,0,1]
	v_mul_f32_e32 v84, v84, v9
	v_mul_f32_e32 v85, v85, v9
	v_mul_f32_e32 v86, v86, v9
	v_mul_f32_e32 v87, v87, v9
	v_mov_b32_e32 v31, v10
	v_cvt_pk_fp8_f32 v31, v84, v85
	v_cvt_pk_fp8_f32 v30, v82, v83 op_sel:[0,0,1]
	v_mul_f32_e32 v88, v88, v9
	v_mul_f32_e32 v89, v89, v9
	v_mul_f32_e32 v90, v90, v9
	v_mul_f32_e32 v91, v91, v9
	v_mov_b32_e32 v32, v10
	v_cvt_pk_fp8_f32 v32, v88, v89
	v_cvt_pk_fp8_f32 v31, v86, v87 op_sel:[0,0,1]
	v_mul_f32_e32 v92, v92, v9
	v_mul_f32_e32 v93, v93, v9
	v_mul_f32_e32 v94, v94, v9
	v_mul_f32_e32 v95, v95, v9
	v_mov_b32_e32 v33, v10
	v_cvt_pk_fp8_f32 v33, v92, v93
	v_cvt_pk_fp8_f32 v32, v90, v91 op_sel:[0,0,1]
	v_mul_f32_e32 v96, v96, v9
	v_mul_f32_e32 v97, v97, v9
	v_mul_f32_e32 v98, v98, v9
	v_mul_f32_e32 v99, v99, v9
	v_mov_b32_e32 v34, v10
	v_cvt_pk_fp8_f32 v34, v96, v97
	v_cvt_pk_fp8_f32 v33, v94, v95 op_sel:[0,0,1]
	v_mul_f32_e32 v100, v100, v9
	v_mul_f32_e32 v101, v101, v9
	v_mul_f32_e32 v102, v102, v9
	v_mul_f32_e32 v103, v103, v9
	v_mov_b32_e32 v35, v10
	v_cvt_pk_fp8_f32 v35, v100, v101
	v_cvt_pk_fp8_f32 v34, v98, v99 op_sel:[0,0,1]
	v_cvt_pk_fp8_f32 v35, v102, v103 op_sel:[0,0,1]
	s_nop 0
	v_mul_f32_e32 v8, 0x3b800000, v6
	global_store_dword v2, v20, s[8:9]
	global_store_dword v2, v21, s[8:9] offset:256
	global_store_dword v2, v22, s[8:9] offset:512
	global_store_dword v2, v23, s[8:9] offset:768
	global_store_dword v2, v24, s[8:9] offset:1024
	global_store_dword v2, v25, s[8:9] offset:1280
	global_store_dword v2, v26, s[8:9] offset:1536
	global_store_dword v2, v27, s[8:9] offset:1792
	global_store_dword v2, v28, s[8:9] offset:2048
	global_store_dword v2, v29, s[8:9] offset:2304
	global_store_dword v2, v30, s[8:9] offset:2560
	global_store_dword v2, v31, s[8:9] offset:2816
	global_store_dword v2, v32, s[8:9] offset:3072
	global_store_dword v2, v33, s[8:9] offset:3328
	global_store_dword v2, v34, s[8:9] offset:3584
	global_store_dword v2, v35, s[8:9] offset:3840
	s_mov_b64 s[18:19], exec
	s_mov_b64 exec, s[12:13]
	global_store_dword v10, v8, s[10:11]
	s_mov_b64 exec, s[18:19]
	s_mov_b32 s4, s5
	s_waitcnt vmcnt(32)
; __device__ __forceinline__ void peer_row_load(f32x4 (&v)[16], const float* const (&in)[34], int it, int layer, int lane) {
;     const int tbl = it >= NEXP, r = it - tbl * NEXP + layer * NEXP;
;     const f32x4* src = (const f32x4*)((tbl ? in[33] : in[32]) + (size_t)r * D) + lane;
; #pragma unroll
;     for (int j = 0; j < 16; ++j) v[j] = src[64 * j];
; }
; __device__ __forceinline__ void peer_row_store(const f32x4 (&v)[16], unsigned char* ws, int it, int layer, int lane) {
;     const int tbl = it >= NEXP, r = it - tbl * NEXP + layer * NEXP;
;     float am = 0.f;
; #pragma unroll
;     for (int j = 0; j < 16; ++j) am = fmaxf(fmaxf(am, fmaxf(fabsf(v[j][0]), fabsf(v[j][1]))), fmaxf(fabsf(v[j][2]), fabsf(v[j][3])));
;     am = __uint_as_float(max64u(__float_as_uint(am)));
	v_max3_f32 v6, |v104|, |v105|, 0
	v_max3_f32 v6, |v106|, |v107|, v6
	s_waitcnt vmcnt(31)
	v_max3_f32 v6, |v108|, |v109|, v6
	v_max3_f32 v6, |v110|, |v111|, v6
	s_waitcnt vmcnt(30)
	v_max3_f32 v6, |v112|, |v113|, v6
	v_max3_f32 v6, |v114|, |v115|, v6
	s_waitcnt vmcnt(29)
	v_max3_f32 v6, |v116|, |v117|, v6
	v_max3_f32 v6, |v118|, |v119|, v6
	s_waitcnt vmcnt(28)
	v_max3_f32 v6, |v120|, |v121|, v6
	v_max3_f32 v6, |v122|, |v123|, v6
	s_waitcnt vmcnt(27)
	v_max3_f32 v6, |v124|, |v125|, v6
	v_max3_f32 v6, |v126|, |v127|, v6
	s_waitcnt vmcnt(26)
	v_max3_f32 v6, |v128|, |v129|, v6
	v_max3_f32 v6, |v130|, |v131|, v6
	s_waitcnt vmcnt(25)
	v_max3_f32 v6, |v132|, |v133|, v6
	v_max3_f32 v6, |v134|, |v135|, v6
	s_waitcnt vmcnt(24)
	v_max3_f32 v6, |v136|, |v137|, v6
	v_max3_f32 v6, |v138|, |v139|, v6
	s_waitcnt vmcnt(23)
	v_max3_f32 v6, |v140|, |v141|, v6
	v_max3_f32 v6, |v142|, |v143|, v6
	s_waitcnt vmcnt(22)
	v_max3_f32 v6, |v144|, |v145|, v6
	v_max3_f32 v6, |v146|, |v147|, v6
	s_waitcnt vmcnt(21)
	v_max3_f32 v6, |v148|, |v149|, v6
	v_max3_f32 v6, |v150|, |v151|, v6
	s_waitcnt vmcnt(20)
	v_max3_f32 v6, |v152|, |v153|, v6
	v_max3_f32 v6, |v154|, |v155|, v6
	s_waitcnt vmcnt(19)
	v_max3_f32 v6, |v156|, |v157|, v6
	v_max3_f32 v6, |v158|, |v159|, v6
	s_waitcnt vmcnt(18)
	v_max3_f32 v6, |v160|, |v161|, v6
	v_max3_f32 v6, |v162|, |v163|, v6
	s_waitcnt vmcnt(17)
; template <int CTRL> __device__ __forceinline__ unsigned dppu(unsigned x) { return (unsigned)__builtin_amdgcn_mov_dpp((int)x, CTRL, 0xf, 0xf, true); }
; __device__ __forceinline__ unsigned max64u(unsigned x) {
;     x = umax_u(x, dppu<DPP_XOR1>(x)); x = umax_u(x, dppu<DPP_XOR2>(x)); x = umax_u(x, dppu<DPP_HMIRROR>(x)); x = umax_u(x, dppu<DPP_MIRROR>(x));
;     auto s = __builtin_amdgcn_permlane16_swap(x, x, false, false); x = umax_u(s[0], s[1]);
;     auto t = __builtin_amdgcn_permlane32_swap(x, x, false, false); return umax_u(t[0], t[1]);
; }
; __device__ __forceinline__ void peer_row_store(const f32x4 (&v)[16], unsigned char* ws, int it, int layer, int lane) {
;     const int tbl = it >= NEXP, r = it - tbl * NEXP + layer * NEXP;
;     float am = 0.f;
; #pragma unroll
;     for (int j = 0; j < 16; ++j) am = fmaxf(fmaxf(am, fmaxf(fabsf(v[j][0]), fabsf(v[j][1]))), fmaxf(fabsf(v[j][2]), fabsf(v[j][3])));
;     am = __uint_as_float(max64u(__float_as_uint(am)));
;     const float q = am > 0.f ? 256.0f / am : 0.f;
;     unsigned* dst = (unsigned*)(ws + (tbl ? WS_PV : WS_PU) + (size_t)r * D) + lane;
;     if (tbl) {
;         const int rl = it - NEXP;
;         unsigned char* pvl = ws + WS_PV + (size_t)layer * NEXP * D + (size_t)rl * 8 + (lane & 1) * 4;
;         unsigned char* pvg = ws + WS_PV + (size_t)layer * NEXP * D + (size_t)NEXP * 2048 + (size_t)rl * 2048 + 4 * lane;
; #pragma unroll
;         for (int j = 0; j < 16; ++j) { int w = __builtin_amdgcn_cvt_pk_bf8_f32(v[j][0] * q, v[j][1] * q, 0, false); w = __builtin_amdgcn_cvt_pk_bf8_f32(v[j][2] * q, v[j][3] * q, w, true);
;             if (j < 8) *(unsigned*)(pvl + (size_t)((lane >> 1) + 32 * j) * (NEXP * 8)) = (unsigned)w;
;             else *(unsigned*)(pvg + 256 * (j - 8)) = (unsigned)w; }
;     } else {
; #pragma unroll
;         for (int j = 0; j < 16; ++j) { int w = __builtin_amdgcn_cvt_pk_fp8_f32(v[j][0] * q, v[j][1] * q, 0, false); w = __builtin_amdgcn_cvt_pk_fp8_f32(v[j][2] * q, v[j][3] * q, w, true); dst[64 * j] = (unsigned)w; }
;     }
;     if (lane == 0) ((float*)(ws + (tbl ? WS_SV : WS_SU)))[r] = am * (1.0f / 256.0f);
; }
	v_max3_f32 v6, |v164|, |v165|, v6
	v_max3_f32 v6, |v166|, |v167|, v6
	s_nop 1
	v_max_u32_dpp v6, v6, v6 quad_perm:[1,0,3,2] row_mask:0xf bank_mask:0xf bound_ctrl:1
	s_nop 1
	v_max_u32_dpp v6, v6, v6 quad_perm:[2,3,0,1] row_mask:0xf bank_mask:0xf bound_ctrl:1
	s_nop 1
	v_max_u32_dpp v6, v6, v6 row_half_mirror row_mask:0xf bank_mask:0xf bound_ctrl:1
	s_nop 1
	v_max_u32_dpp v6, v6, v6 row_mirror row_mask:0xf bank_mask:0xf bound_ctrl:1
	s_nop 1
	v_mov_b32_e32 v7, v6
	s_nop 1
	v_permlane16_swap_b32_e32 v6, v7
	v_max_u32_e32 v6, v6, v7
	v_mov_b32_e32 v7, v6
	s_nop 1
	v_permlane32_swap_b32_e32 v6, v7
	v_max_u32_e32 v6, v6, v7
	v_div_scale_f32 v12, s[16:17], v6, v6, s14
	v_rcp_f32_e32 v13, v12
	s_nop 0
	v_fma_f32 v14, -v12, v13, 1.0
	v_fmac_f32_e32 v13, v14, v13
	v_div_scale_f32 v14, vcc, s14, v6, s14
	v_mul_f32_e32 v15, v14, v13
	v_fma_f32 v16, -v12, v15, v14
	v_fmac_f32_e32 v15, v16, v13
	v_fma_f32 v12, -v12, v15, v14
	v_div_fmas_f32 v12, v12, v13, v15
	v_div_fixup_f32 v9, v12, v6, s14
	v_cmp_lt_f32_e32 vcc, 0, v6
	s_nop 1
	v_cndmask_b32_e32 v9, 0, v9, vcc
	s_lshl_b32 s1, s4, 12
	s_add_u32 s8, s90, 0xba00000
	s_addc_u32 s9, s91, 0
	s_add_u32 s8, s8, s1
	s_addc_u32 s9, s9, 0
	s_lshl_b32 s1, s4, 2
	s_add_u32 s10, s90, 0x1ba00000
	s_addc_u32 s11, s91, 0
	s_add_u32 s10, s10, s1
	s_addc_u32 s11, s11, 0
	v_mul_f32_e32 v104, v104, v9
	v_mul_f32_e32 v105, v105, v9
	v_mul_f32_e32 v106, v106, v9
	v_mul_f32_e32 v107, v107, v9
	v_mov_b32_e32 v20, v10
	v_cvt_pk_fp8_f32 v20, v104, v105
	v_mul_f32_e32 v108, v108, v9
	v_mul_f32_e32 v109, v109, v9
	v_mul_f32_e32 v110, v110, v9
	v_mul_f32_e32 v111, v111, v9
	v_mov_b32_e32 v21, v10
	v_cvt_pk_fp8_f32 v21, v108, v109
	v_cvt_pk_fp8_f32 v20, v106, v107 op_sel:[0,0,1]
	v_mul_f32_e32 v112, v112, v9
	v_mul_f32_e32 v113, v113, v9
	v_mul_f32_e32 v114, v114, v9
	v_mul_f32_e32 v115, v115, v9
	v_mov_b32_e32 v22, v10
	v_cvt_pk_fp8_f32 v22, v112, v113
	v_cvt_pk_fp8_f32 v21, v110, v111 op_sel:[0,0,1]
	v_mul_f32_e32 v116, v116, v9
	v_mul_f32_e32 v117, v117, v9
	v_mul_f32_e32 v118, v118, v9
	v_mul_f32_e32 v119, v119, v9
	v_mov_b32_e32 v23, v10
	v_cvt_pk_fp8_f32 v23, v116, v117
	v_cvt_pk_fp8_f32 v22, v114, v115 op_sel:[0,0,1]
	v_mul_f32_e32 v120, v120, v9
	v_mul_f32_e32 v121, v121, v9
	v_mul_f32_e32 v122, v122, v9
	v_mul_f32_e32 v123, v123, v9
	v_mov_b32_e32 v24, v10
	v_cvt_pk_fp8_f32 v24, v120, v121
	v_cvt_pk_fp8_f32 v23, v118, v119 op_sel:[0,0,1]
	v_mul_f32_e32 v124, v124, v9
	v_mul_f32_e32 v125, v125, v9
	v_mul_f32_e32 v126, v126, v9
	v_mul_f32_e32 v127, v127, v9
	v_mov_b32_e32 v25, v10
	v_cvt_pk_fp8_f32 v25, v124, v125
	v_cvt_pk_fp8_f32 v24, v122, v123 op_sel:[0,0,1]
	v_mul_f32_e32 v128, v128, v9
	v_mul_f32_e32 v129, v129, v9
	v_mul_f32_e32 v130, v130, v9
	v_mul_f32_e32 v131, v131, v9
	v_mov_b32_e32 v26, v10
	v_cvt_pk_fp8_f32 v26, v128, v129
	v_cvt_pk_fp8_f32 v25, v126, v127 op_sel:[0,0,1]
	v_mul_f32_e32 v132, v132, v9
	v_mul_f32_e32 v133, v133, v9
	v_mul_f32_e32 v134, v134, v9
	v_mul_f32_e32 v135, v135, v9
	v_mov_b32_e32 v27, v10
	v_cvt_pk_fp8_f32 v27, v132, v133
	v_cvt_pk_fp8_f32 v26, v130, v131 op_sel:[0,0,1]
	v_mul_f32_e32 v136, v136, v9
	v_mul_f32_e32 v137, v137, v9
	v_mul_f32_e32 v138, v138, v9
	v_mul_f32_e32 v139, v139, v9
	v_mov_b32_e32 v28, v10
	v_cvt_pk_fp8_f32 v28, v136, v137
	v_cvt_pk_fp8_f32 v27, v134, v135 op_sel:[0,0,1]
	v_mul_f32_e32 v140, v140, v9
	v_mul_f32_e32 v141, v141, v9
	v_mul_f32_e32 v142, v142, v9
	v_mul_f32_e32 v143, v143, v9
	v_mov_b32_e32 v29, v10
	v_cvt_pk_fp8_f32 v29, v140, v141
	v_cvt_pk_fp8_f32 v28, v138, v139 op_sel:[0,0,1]
	v_mul_f32_e32 v144, v144, v9
	v_mul_f32_e32 v145, v145, v9
	v_mul_f32_e32 v146, v146, v9
	v_mul_f32_e32 v147, v147, v9
	v_mov_b32_e32 v30, v10
	v_cvt_pk_fp8_f32 v30, v144, v145
	v_cvt_pk_fp8_f32 v29, v142, v143 op_sel:[0,0,1]
	v_mul_f32_e32 v148, v148, v9
	v_mul_f32_e32 v149, v149, v9
	v_mul_f32_e32 v150, v150, v9
	v_mul_f32_e32 v151, v151, v9
	v_mov_b32_e32 v31, v10
	v_cvt_pk_fp8_f32 v31, v148, v149
	v_cvt_pk_fp8_f32 v30, v146, v147 op_sel:[0,0,1]
	v_mul_f32_e32 v152, v152, v9
	v_mul_f32_e32 v153, v153, v9
	v_mul_f32_e32 v154, v154, v9
	v_mul_f32_e32 v155, v155, v9
	v_mov_b32_e32 v32, v10
	v_cvt_pk_fp8_f32 v32, v152, v153
	v_cvt_pk_fp8_f32 v31, v150, v151 op_sel:[0,0,1]
	v_mul_f32_e32 v156, v156, v9
	v_mul_f32_e32 v157, v157, v9
	v_mul_f32_e32 v158, v158, v9
	v_mul_f32_e32 v159, v159, v9
	v_mov_b32_e32 v33, v10
	v_cvt_pk_fp8_f32 v33, v156, v157
	v_cvt_pk_fp8_f32 v32, v154, v155 op_sel:[0,0,1]
	v_mul_f32_e32 v160, v160, v9
	v_mul_f32_e32 v161, v161, v9
	v_mul_f32_e32 v162, v162, v9
	v_mul_f32_e32 v163, v163, v9
	v_mov_b32_e32 v34, v10
	v_cvt_pk_fp8_f32 v34, v160, v161
	v_cvt_pk_fp8_f32 v33, v158, v159 op_sel:[0,0,1]
	v_mul_f32_e32 v164, v164, v9
	v_mul_f32_e32 v165, v165, v9
	v_mul_f32_e32 v166, v166, v9
	v_mul_f32_e32 v167, v167, v9
	v_mov_b32_e32 v35, v10
	v_cvt_pk_fp8_f32 v35, v164, v165
	v_cvt_pk_fp8_f32 v34, v162, v163 op_sel:[0,0,1]
	v_cvt_pk_fp8_f32 v35, v166, v167 op_sel:[0,0,1]
	s_nop 0
	v_mul_f32_e32 v8, 0x3b800000, v6
	global_store_dword v2, v20, s[8:9]
	global_store_dword v2, v21, s[8:9] offset:256
	global_store_dword v2, v22, s[8:9] offset:512
	global_store_dword v2, v23, s[8:9] offset:768
	global_store_dword v2, v24, s[8:9] offset:1024
	global_store_dword v2, v25, s[8:9] offset:1280
	global_store_dword v2, v26, s[8:9] offset:1536
	global_store_dword v2, v27, s[8:9] offset:1792
	global_store_dword v2, v28, s[8:9] offset:2048
	global_store_dword v2, v29, s[8:9] offset:2304
	global_store_dword v2, v30, s[8:9] offset:2560
	global_store_dword v2, v31, s[8:9] offset:2816
	global_store_dword v2, v32, s[8:9] offset:3072
	global_store_dword v2, v33, s[8:9] offset:3328
	global_store_dword v2, v34, s[8:9] offset:3584
	global_store_dword v2, v35, s[8:9] offset:3840
	s_mov_b64 s[18:19], exec
	s_mov_b64 exec, s[12:13]
	global_store_dword v10, v8, s[10:11]
	s_mov_b64 exec, s[18:19]
	s_waitcnt vmcnt(0)
